# prep f32-MFMA projections: rolling ds_read prefetch in the MFMA shadow, next matrix's fragments issued before the write-back, product read-backs deferred (counted lgkmcnt)
# speedup vs baseline: 1.0033x; 1.0033x over previous
.Lmy_pp_a:
	v_and_b32_e32 v34, 1, v3
	v_lshlrev_b32_e32 v34, 4, v34
	v_lshl_add_u32 v34, v2, 7, v34
	v_add_u32_e32 v34, s3, v34
	v_lshlrev_b32_e32 v110, 5, v203
	v_add_u32_e32 v110, s3, v110
	v_add_u32_e32 v108, 0x2000, v5
	ds_read_b128 v[114:117], v4 offset:256
	ds_read_b128 v[118:121], v4 offset:272
	ds_read_b128 v[122:125], v108 offset:0
	ds_read_b128 v[126:129], v108 offset:1024
	ds_read_b128 v[130:133], v108 offset:2048
	ds_read_b128 v[170:173], v108 offset:3072
	s_waitcnt lgkmcnt(3)
	v_mfma_f32_16x16x4_f32 v[6:9], v114, v122, 0
	v_mfma_f32_16x16x4_f32 v[10:13], v114, v123, 0
	v_mfma_f32_16x16x4_f32 v[14:17], v114, v124, 0
	v_mfma_f32_16x16x4_f32 v[94:97], v114, v125, 0
	s_waitcnt lgkmcnt(2)
	v_mfma_f32_16x16x4_f32 v[6:9], v115, v126, v[6:9]
	v_mfma_f32_16x16x4_f32 v[10:13], v115, v127, v[10:13]
	v_mfma_f32_16x16x4_f32 v[14:17], v115, v128, v[14:17]
	v_mfma_f32_16x16x4_f32 v[94:97], v115, v129, v[94:97]
	ds_read_b128 v[122:125], v108 offset:4096
	s_waitcnt lgkmcnt(2)
	v_mfma_f32_16x16x4_f32 v[6:9], v116, v130, v[6:9]
	v_mfma_f32_16x16x4_f32 v[10:13], v116, v131, v[10:13]
	v_mfma_f32_16x16x4_f32 v[14:17], v116, v132, v[14:17]
	v_mfma_f32_16x16x4_f32 v[94:97], v116, v133, v[94:97]
	ds_read_b128 v[126:129], v108 offset:5120
	s_waitcnt lgkmcnt(2)
	v_mfma_f32_16x16x4_f32 v[6:9], v117, v170, v[6:9]
	v_mfma_f32_16x16x4_f32 v[10:13], v117, v171, v[10:13]
	v_mfma_f32_16x16x4_f32 v[14:17], v117, v172, v[14:17]
	v_mfma_f32_16x16x4_f32 v[94:97], v117, v173, v[94:97]
	ds_read_b128 v[130:133], v108 offset:6144
	s_waitcnt lgkmcnt(2)
	v_mfma_f32_16x16x4_f32 v[6:9], v118, v122, v[6:9]
	v_mfma_f32_16x16x4_f32 v[10:13], v118, v123, v[10:13]
	v_mfma_f32_16x16x4_f32 v[14:17], v118, v124, v[14:17]
	v_mfma_f32_16x16x4_f32 v[94:97], v118, v125, v[94:97]
	ds_read_b128 v[170:173], v108 offset:7168
	s_waitcnt lgkmcnt(2)
	v_mfma_f32_16x16x4_f32 v[6:9], v119, v126, v[6:9]
	v_mfma_f32_16x16x4_f32 v[10:13], v119, v127, v[10:13]
	v_mfma_f32_16x16x4_f32 v[14:17], v119, v128, v[14:17]
	v_mfma_f32_16x16x4_f32 v[94:97], v119, v129, v[94:97]
	s_waitcnt lgkmcnt(1)
	v_mfma_f32_16x16x4_f32 v[6:9], v120, v130, v[6:9]
	v_mfma_f32_16x16x4_f32 v[10:13], v120, v131, v[10:13]
	v_mfma_f32_16x16x4_f32 v[14:17], v120, v132, v[14:17]
	v_mfma_f32_16x16x4_f32 v[94:97], v120, v133, v[94:97]
	s_waitcnt lgkmcnt(0)
	v_mfma_f32_16x16x4_f32 v[6:9], v121, v170, v[6:9]
	v_mfma_f32_16x16x4_f32 v[10:13], v121, v171, v[10:13]
	v_mfma_f32_16x16x4_f32 v[14:17], v121, v172, v[14:17]
	v_mfma_f32_16x16x4_f32 v[94:97], v121, v173, v[94:97]
	s_nop 3
	v_add_u32_e32 v108, 0xa000, v5
	ds_read_b128 v[114:117], v4 offset:0
	ds_read_b128 v[118:121], v4 offset:16
	ds_read_b128 v[122:125], v108 offset:0
	ds_read_b128 v[126:129], v108 offset:1024
	ds_read_b128 v[130:133], v108 offset:2048
	ds_read_b128 v[170:173], v108 offset:3072
	s_nop 15
	s_nop 15
	s_cmp_lt_u32 s2, 4
	s_cselect_b32 exec_lo, -1, 0
	s_cselect_b32 exec_hi, 0, -1
	ds_write_b128 v34, v[6:9] offset:0
	ds_write_b128 v34, v[10:13] offset:32
	ds_write_b128 v34, v[14:17] offset:64
	ds_write_b128 v34, v[94:97] offset:96
	s_mov_b64 exec, -1
	ds_read_b128 v[174:177], v110
	ds_read_b128 v[178:181], v110 offset:16
	s_waitcnt lgkmcnt(9)
	v_mfma_f32_16x16x4_f32 v[6:9], v114, v122, 0
	v_mfma_f32_16x16x4_f32 v[10:13], v114, v123, 0
	v_mfma_f32_16x16x4_f32 v[14:17], v114, v124, 0
	v_mfma_f32_16x16x4_f32 v[94:97], v114, v125, 0
	s_waitcnt lgkmcnt(8)
	v_mfma_f32_16x16x4_f32 v[6:9], v115, v126, v[6:9]
	v_mfma_f32_16x16x4_f32 v[10:13], v115, v127, v[10:13]
	v_mfma_f32_16x16x4_f32 v[14:17], v115, v128, v[14:17]
	v_mfma_f32_16x16x4_f32 v[94:97], v115, v129, v[94:97]
	ds_read_b128 v[122:125], v108 offset:4096
	s_waitcnt lgkmcnt(8)
	v_mfma_f32_16x16x4_f32 v[6:9], v116, v130, v[6:9]
	v_mfma_f32_16x16x4_f32 v[10:13], v116, v131, v[10:13]
	v_mfma_f32_16x16x4_f32 v[14:17], v116, v132, v[14:17]
	v_mfma_f32_16x16x4_f32 v[94:97], v116, v133, v[94:97]
	ds_read_b128 v[126:129], v108 offset:5120
	s_waitcnt lgkmcnt(8)
	v_mfma_f32_16x16x4_f32 v[6:9], v117, v170, v[6:9]
	v_mfma_f32_16x16x4_f32 v[10:13], v117, v171, v[10:13]
	v_mfma_f32_16x16x4_f32 v[14:17], v117, v172, v[14:17]
	v_mfma_f32_16x16x4_f32 v[94:97], v117, v173, v[94:97]
	ds_read_b128 v[130:133], v108 offset:6144
	s_waitcnt lgkmcnt(2)
	v_mfma_f32_16x16x4_f32 v[6:9], v118, v122, v[6:9]
	v_mfma_f32_16x16x4_f32 v[10:13], v118, v123, v[10:13]
	v_mfma_f32_16x16x4_f32 v[14:17], v118, v124, v[14:17]
	v_mfma_f32_16x16x4_f32 v[94:97], v118, v125, v[94:97]
	ds_read_b128 v[170:173], v108 offset:7168
	s_waitcnt lgkmcnt(2)
	v_mfma_f32_16x16x4_f32 v[6:9], v119, v126, v[6:9]
	v_mfma_f32_16x16x4_f32 v[10:13], v119, v127, v[10:13]
	v_mfma_f32_16x16x4_f32 v[14:17], v119, v128, v[14:17]
	v_mfma_f32_16x16x4_f32 v[94:97], v119, v129, v[94:97]
	s_waitcnt lgkmcnt(1)
	v_mfma_f32_16x16x4_f32 v[6:9], v120, v130, v[6:9]
	v_mfma_f32_16x16x4_f32 v[10:13], v120, v131, v[10:13]
	v_mfma_f32_16x16x4_f32 v[14:17], v120, v132, v[14:17]
	v_mfma_f32_16x16x4_f32 v[94:97], v120, v133, v[94:97]
	s_waitcnt lgkmcnt(0)
	v_mfma_f32_16x16x4_f32 v[6:9], v121, v170, v[6:9]
	v_mfma_f32_16x16x4_f32 v[10:13], v121, v171, v[10:13]
	v_mfma_f32_16x16x4_f32 v[14:17], v121, v172, v[14:17]
	v_mfma_f32_16x16x4_f32 v[94:97], v121, v173, v[94:97]
	s_nop 3
	v_add_u32_e32 v108, 0x12000, v5
	ds_read_b128 v[114:117], v4 offset:128
	ds_read_b128 v[118:121], v4 offset:144
	ds_read_b128 v[122:125], v108 offset:0
	ds_read_b128 v[126:129], v108 offset:1024
	ds_read_b128 v[130:133], v108 offset:2048
	ds_read_b128 v[170:173], v108 offset:3072
	s_nop 15
	s_nop 15
	s_cmp_lt_u32 s2, 4
	s_cselect_b32 exec_lo, -1, 0
	s_cselect_b32 exec_hi, 0, -1
	ds_write_b128 v34, v[6:9] offset:0
	ds_write_b128 v34, v[10:13] offset:32
	ds_write_b128 v34, v[14:17] offset:64
	ds_write_b128 v34, v[94:97] offset:96
	s_mov_b64 exec, -1
	ds_read_b128 v[182:185], v110
	ds_read_b128 v[186:189], v110 offset:16
	s_waitcnt lgkmcnt(9)
	v_mfma_f32_16x16x4_f32 v[6:9], v114, v122, 0
	v_mfma_f32_16x16x4_f32 v[10:13], v114, v123, 0
	v_mfma_f32_16x16x4_f32 v[14:17], v114, v124, 0
	v_mfma_f32_16x16x4_f32 v[94:97], v114, v125, 0
	s_waitcnt lgkmcnt(8)
	v_mfma_f32_16x16x4_f32 v[6:9], v115, v126, v[6:9]
	v_mfma_f32_16x16x4_f32 v[10:13], v115, v127, v[10:13]
	v_mfma_f32_16x16x4_f32 v[14:17], v115, v128, v[14:17]
	v_mfma_f32_16x16x4_f32 v[94:97], v115, v129, v[94:97]
	ds_read_b128 v[122:125], v108 offset:4096
	s_waitcnt lgkmcnt(8)
	v_mfma_f32_16x16x4_f32 v[6:9], v116, v130, v[6:9]
	v_mfma_f32_16x16x4_f32 v[10:13], v116, v131, v[10:13]
	v_mfma_f32_16x16x4_f32 v[14:17], v116, v132, v[14:17]
	v_mfma_f32_16x16x4_f32 v[94:97], v116, v133, v[94:97]
	ds_read_b128 v[126:129], v108 offset:5120
	s_waitcnt lgkmcnt(8)
	v_mfma_f32_16x16x4_f32 v[6:9], v117, v170, v[6:9]
	v_mfma_f32_16x16x4_f32 v[10:13], v117, v171, v[10:13]
	v_mfma_f32_16x16x4_f32 v[14:17], v117, v172, v[14:17]
	v_mfma_f32_16x16x4_f32 v[94:97], v117, v173, v[94:97]
	ds_read_b128 v[130:133], v108 offset:6144
	s_waitcnt lgkmcnt(2)
	v_mfma_f32_16x16x4_f32 v[6:9], v118, v122, v[6:9]
	v_mfma_f32_16x16x4_f32 v[10:13], v118, v123, v[10:13]
	v_mfma_f32_16x16x4_f32 v[14:17], v118, v124, v[14:17]
	v_mfma_f32_16x16x4_f32 v[94:97], v118, v125, v[94:97]
	ds_read_b128 v[170:173], v108 offset:7168
	s_waitcnt lgkmcnt(2)
	v_mfma_f32_16x16x4_f32 v[6:9], v119, v126, v[6:9]
	v_mfma_f32_16x16x4_f32 v[10:13], v119, v127, v[10:13]
	v_mfma_f32_16x16x4_f32 v[14:17], v119, v128, v[14:17]
	v_mfma_f32_16x16x4_f32 v[94:97], v119, v129, v[94:97]
	s_waitcnt lgkmcnt(1)
	v_mfma_f32_16x16x4_f32 v[6:9], v120, v130, v[6:9]
	v_mfma_f32_16x16x4_f32 v[10:13], v120, v131, v[10:13]
	v_mfma_f32_16x16x4_f32 v[14:17], v120, v132, v[14:17]
	v_mfma_f32_16x16x4_f32 v[94:97], v120, v133, v[94:97]
	s_waitcnt lgkmcnt(0)
	v_mfma_f32_16x16x4_f32 v[6:9], v121, v170, v[6:9]
	v_mfma_f32_16x16x4_f32 v[10:13], v121, v171, v[10:13]
	v_mfma_f32_16x16x4_f32 v[14:17], v121, v172, v[14:17]
	v_mfma_f32_16x16x4_f32 v[94:97], v121, v173, v[94:97]
	s_nop 3
	s_nop 15
	s_nop 15
	s_cmp_lt_u32 s2, 4
	s_cselect_b32 exec_lo, -1, 0
	s_cselect_b32 exec_hi, 0, -1
	ds_write_b128 v34, v[6:9] offset:0
	ds_write_b128 v34, v[10:13] offset:32
	ds_write_b128 v34, v[14:17] offset:64
	ds_write_b128 v34, v[94:97] offset:96
	s_mov_b64 exec, -1
	ds_read_b128 v[122:125], v110
	ds_read_b128 v[126:129], v110 offset:16
	s_waitcnt lgkmcnt(0)
	v_add_f32_e32 v102, v138, v174
	v_add_f32_e32 v103, v138, v175
	v_add_f32_e32 v16, v138, v176
	v_add_f32_e32 v17, v138, v177
	v_add_f32_e32 v10, v138, v178
	v_add_f32_e32 v11, v138, v179
	v_add_f32_e32 v96, v138, v180
	v_add_f32_e32 v97, v138, v181
	v_add_f32_e32 v107, v134, v182
	v_add_f32_e32 v106, v134, v183
	v_add_f32_e32 v13, v134, v184
	v_add_f32_e32 v12, v134, v185
	v_add_f32_e32 v8, v134, v186
	v_add_f32_e32 v9, v134, v187
	v_add_f32_e32 v94, v134, v188
	v_add_f32_e32 v95, v134, v189
	v_add_f32_e32 v105, v136, v122
	v_add_f32_e32 v104, v136, v123
	v_add_f32_e32 v15, v136, v124
	v_add_f32_e32 v14, v136, v125
	v_add_f32_e32 v7, v136, v126
	v_add_f32_e32 v6, v136, v127
	v_add_f32_e32 v91, v136, v128
	v_add_f32_e32 v90, v136, v129
	s_mov_b32 s2, 0
	v_lshlrev_b32_e32 v2, 16, v157
	v_cndmask_b32_e64 v123, 0, v2, s[40:41]
	v_lshlrev_b32_e32 v2, 16, v154
	v_cndmask_b32_e32 v126, 0, v2, vcc
	v_lshlrev_b32_e32 v2, 16, v152
	v_cndmask_b32_e32 v127, 0, v2, vcc
	global_load_dword v2, v[32:33], off offset:1024
	global_load_dword v3, v[40:41], off
	global_load_dword v4, v[36:37], off
	global_load_dword v5, v[38:39], off
	global_load_dword v110, v[32:33], off offset:3712
	global_load_dword v108, v[32:33], off offset:2048
	global_load_dword v112, v[32:33], off
	v_lshlrev_b32_e32 v34, 16, v160
	v_cndmask_b32_e64 v128, 0, v34, s[42:43]
	v_lshlrev_b32_e32 v81, 16, v81
	v_lshlrev_b32_e32 v34, 16, v83
	v_cndmask_b32_e32 v129, 0, v34, vcc
	v_lshlrev_b32_e32 v34, 16, v144
	v_cndmask_b32_e32 v144, 0, v81, vcc
	global_load_dword v81, v[42:43], off
	v_lshlrev_b32_e32 v116, 16, v153
	v_cndmask_b32_e64 v130, 0, v34, s[44:45]
	v_lshlrev_b32_e32 v34, 16, v109
	v_lshlrev_b32_e32 v89, 16, v89
	v_lshlrev_b32_e32 v114, 16, v156
	v_cndmask_b32_e64 v83, 0, v34, s[46:47]
	v_lshlrev_b32_e32 v34, 16, v93
	v_lshlrev_b32_e32 v93, 16, v99
	v_cndmask_b32_e32 v133, 0, v116, vcc
	v_cndmask_b32_e64 v116, 0, v89, s[48:49]
	v_and_b32_e32 v89, 64, v203
	v_lshlrev_b32_e32 v117, 16, v155
	v_lshlrev_b32_e32 v118, 16, v151
	v_lshlrev_b32_e32 v119, 16, v161
	v_lshlrev_b32_e32 v85, 16, v85
	v_lshlrev_b32_e32 v79, 16, v79
	v_lshlrev_b32_e32 v109, 16, v111
	v_cndmask_b32_e64 v111, 0, v34, s[48:49]
	v_lshlrev_b32_e32 v99, 16, v148
	v_lshlrev_b32_e32 v34, 16, v149
	v_lshlrev_b32_e32 v122, 16, v150
	v_cndmask_b32_e64 v131, 0, v114, s[40:41]
	v_cndmask_b32_e64 v114, 0, v93, s[48:49]
	v_add_u32_e32 v89, 64, v89
	v_xor_b32_e32 v93, 1, v203
	v_cndmask_b32_e32 v34, 0, v34, vcc
	v_lshlrev_b32_e32 v124, 16, v145
	v_cndmask_b32_e32 v134, 0, v117, vcc
	v_cndmask_b32_e32 v136, 0, v118, vcc
	v_cndmask_b32_e32 v138, 0, v119, vcc
	v_cndmask_b32_e32 v85, 0, v85, vcc
	v_cndmask_b32_e64 v145, 0, v79, s[44:45]
	v_cndmask_b32_e64 v148, 0, v109, s[46:47]
	v_cndmask_b32_e32 v109, 0, v99, vcc
	v_cndmask_b32_e32 v79, 0, v122, vcc
	v_cmp_lt_i32_e32 vcc, v93, v89
	v_lshlrev_b32_e32 v121, 16, v113
	v_lshlrev_b32_e32 v113, 16, v146
	v_cndmask_b32_e32 v93, v203, v93, vcc
	v_lshlrev_b32_e32 v122, 2, v93
	v_xor_b32_e32 v93, 2, v203
	v_cmp_lt_i32_e32 vcc, v93, v89
	v_cndmask_b32_e64 v146, 0, v121, s[44:45]
	v_lshlrev_b32_e32 v120, 16, v159
	v_cndmask_b32_e32 v93, v203, v93, vcc
	v_lshlrev_b32_e32 v121, 2, v93
	v_xor_b32_e32 v93, 4, v203
	v_cmp_lt_i32_e32 vcc, v93, v89
	v_cndmask_b32_e64 v140, 0, v120, s[42:43]
	v_sub_f32_e32 v99, v127, v126
	v_cndmask_b32_e32 v93, v203, v93, vcc
	v_lshlrev_b32_e32 v120, 2, v93
	v_xor_b32_e32 v93, 8, v203
	v_cmp_lt_i32_e32 vcc, v93, v89
	v_lshlrev_b32_e32 v101, 16, v101
	v_lshlrev_b32_e32 v125, 16, v147
	v_cndmask_b32_e32 v93, v203, v93, vcc
	v_lshlrev_b32_e32 v119, 2, v93
	v_xor_b32_e32 v93, 16, v203
	v_cmp_lt_i32_e32 vcc, v93, v89
	v_cndmask_b32_e64 v147, 0, v101, s[46:47]
	v_lshlrev_b32_e32 v115, 16, v158
	v_cndmask_b32_e32 v93, v203, v93, vcc
	v_lshlrev_b32_e32 v118, 2, v93
	v_xor_b32_e32 v93, 32, v203
	v_cmp_lt_i32_e32 vcc, v93, v89
	v_cndmask_b32_e64 v132, 0, v115, s[40:41]
	v_cndmask_b32_e64 v115, 0, v125, s[50:51]
	v_cndmask_b32_e32 v89, v203, v93, vcc
	v_sub_f32_e32 v93, v123, v126
	s_waitcnt vmcnt(7)
	v_fma_f32 v93, v93, v2, v126
	s_waitcnt vmcnt(5)
	v_fmac_f32_e32 v93, v99, v4
	v_mul_f32_e32 v99, v93, v3
	v_mul_f32_e32 v101, v99, v99
	s_nop 1
	v_mov_b32_dpp v101, v101 quad_perm:[1,0,3,2] row_mask:0xf bank_mask:0xf
	v_lshlrev_b32_e32 v123, 2, v89
	v_sub_f32_e32 v89, v131, v133
	v_cndmask_b32_e64 v117, 0, v124, s[50:51]
	s_waitcnt vmcnt(1)
	v_fma_f32 v89, v89, v112, v133
	s_waitcnt lgkmcnt(0)
	v_fmac_f32_e32 v101, v99, v99
	s_nop 1
	v_sub_f32_e32 v124, v136, v133
	v_fmac_f32_e32 v89, v124, v110
	v_sub_f32_e32 v124, v132, v134
	v_fma_f32 v131, v124, v108, v134
	s_waitcnt lgkmcnt(0)
	v_add_f32_dpp v101, v101, v101 quad_perm:[2,3,0,1] row_mask:0xf bank_mask:0xf
	s_nop 1
	v_sub_f32_e32 v124, v138, v134
	v_fmac_f32_e32 v131, v124, v5
	v_mul_f32_e32 v102, 0xbfb8aa3b, v102
	v_exp_f32_e32 v102, v102
	s_waitcnt lgkmcnt(0)
	v_add_f32_dpp v101, v101, v101 row_half_mirror row_mask:0xf bank_mask:0xf
	s_nop 1
	v_mul_f32_e32 v107, 0xbfb8aa3b, v107
	v_add_f32_e32 v102, 1.0, v102
	v_rcp_f32_e32 v102, v102
	v_exp_f32_e32 v107, v107
	s_waitcnt lgkmcnt(0)
	v_add_f32_dpp v101, v101, v101 row_mirror row_mask:0xf bank_mask:0xf
	v_mov_b32_e32 v124, v101
	s_nop 1
	v_permlane16_swap_b32_e32 v124, v101
	v_mul_f32_e32 v105, 0xbfb8aa3b, v105
	v_exp_f32_e32 v105, v105
	v_cvt_pk_bf16_f32 v89, v89, s0
	v_add_f32_e32 v107, 1.0, v107
	s_waitcnt lgkmcnt(0)
	v_add_f32_e32 v101, v101, v124
	v_mov_b32_e32 v124, v101
	s_nop 1
	v_permlane32_swap_b32_e32 v124, v101
	v_rcp_f32_e32 v107, v107
	v_add_f32_e32 v105, 1.0, v105
	v_rcp_f32_e32 v105, v105
	v_mul_f32_e32 v103, 0xbfb8aa3b, v103
	s_waitcnt lgkmcnt(0)
	v_add_f32_e32 v101, v101, v124
	v_add_f32_e32 v101, 0x2b8cbccc, v101
	v_rsq_f32_e32 v101, v101
	v_mul_f32_e32 v107, 0xbf1b459e, v107
	v_mul_f32_e32 v107, 0x3fb8aa3b, v107
	v_mul_f32_e32 v105, 0xbf1b459e, v105
	v_mul_f32_e32 v99, v99, v101
	v_add_f32_e32 v101, -1.0, v102
	s_waitcnt vmcnt(0)
	v_fma_f32 v101, v101, v81, 1.0
	v_mul_f32_e32 v93, v93, v101
	v_ashrrev_i32_e32 v101, 31, v100
	v_lshlrev_b64 v[100:101], 9, v[100:101]
	v_or_b32_e32 v100, v100, v31
	v_lshl_add_u64 v[124:125], s[74:75], 0, v[100:101]
	global_store_short v[124:125], v89, off
	v_lshl_add_u64 v[124:125], s[76:77], 0, v[100:101]
	v_cvt_pk_bf16_f32 v89, v93, s0
	global_store_short v[124:125], v89, off
	v_lshl_add_u64 v[124:125], s[78:79], 0, v[100:101]
	v_cvt_pk_bf16_f32 v89, v131, s0
	global_store_short v[124:125], v89, off
	v_lshl_add_u64 v[124:125], s[80:81], 0, v[100:101]
	v_cvt_pk_bf16_f32 v89, v99, s0
	v_sub_f32_e32 v93, v126, v127
	global_store_short v[124:125], v89, off
	v_mul_f32_e32 v89, v102, v99
	v_fma_f32 v93, v93, v2, v127
	v_sub_f32_e32 v99, v128, v127
	v_fmac_f32_e32 v93, v99, v4
	v_mul_f32_e32 v99, v93, v3
	v_mul_f32_e32 v102, v99, v99
	v_exp_f32_e32 v107, v107
	v_mul_f32_e32 v105, 0x3fb8aa3b, v105
	s_nop 1
	v_mov_b32_dpp v102, v102 quad_perm:[1,0,3,2] row_mask:0xf bank_mask:0xf
	v_exp_f32_e32 v105, v105
	v_lshl_add_u64 v[124:125], s[82:83], 0, v[100:101]
	v_cvt_pk_bf16_f32 v89, v89, s0
	global_store_short v[124:125], v89, off
	v_lshl_add_u64 v[124:125], s[84:85], 0, v[100:101]
	v_cvt_pk_bf16_f32 v89, v107, s0
	global_store_short v[124:125], v89, off
	v_lshl_add_u64 v[100:101], s[86:87], 0, v[100:101]
	v_cvt_pk_bf16_f32 v89, v105, s0
	s_waitcnt lgkmcnt(0)
	v_fmac_f32_e32 v102, v99, v99
	global_store_short v[100:101], v89, off
	s_nop 1
	v_mul_f32_e32 v106, 0xbfb8aa3b, v106
	v_sub_f32_e32 v89, v133, v136
	v_exp_f32_e32 v103, v103
	v_exp_f32_e32 v106, v106
	s_waitcnt lgkmcnt(0)
	v_add_f32_dpp v101, v102, v102 quad_perm:[2,3,0,1] row_mask:0xf bank_mask:0xf
	s_nop 1
	v_lshlrev_b32_e32 v87, 16, v87
	v_fma_f32 v89, v89, v112, v136
	v_sub_f32_e32 v100, v140, v136
	v_cndmask_b32_e64 v87, 0, v87, s[42:43]
	s_waitcnt lgkmcnt(0)
	v_add_f32_dpp v101, v101, v101 row_half_mirror row_mask:0xf bank_mask:0xf
	s_nop 1
	v_fmac_f32_e32 v89, v100, v110
	v_sub_f32_e32 v100, v134, v138
	v_fma_f32 v105, v100, v108, v138
	v_sub_f32_e32 v100, v87, v138
	s_waitcnt lgkmcnt(0)
	v_add_f32_dpp v101, v101, v101 row_mirror row_mask:0xf bank_mask:0xf
	v_mov_b32_e32 v102, v101
	s_nop 1
	v_permlane16_swap_b32_e32 v102, v101
	v_fmac_f32_e32 v105, v100, v5
	v_add_f32_e32 v100, 1.0, v103
	v_add_f32_e32 v103, 1.0, v106
	v_rcp_f32_e32 v103, v103
	s_waitcnt lgkmcnt(0)
	v_add_f32_e32 v101, v101, v102
	v_mov_b32_e32 v102, v101
	s_nop 1
	v_permlane32_swap_b32_e32 v102, v101
	v_rcp_f32_e32 v106, v100
	v_mul_f32_e32 v100, 0xbf1b459e, v103
	v_mul_f32_e32 v103, 0xbfb8aa3b, v104
	v_exp_f32_e32 v103, v103
	s_waitcnt lgkmcnt(0)
	v_add_f32_e32 v101, v101, v102
	v_add_f32_e32 v101, 0x2b8cbccc, v101
	v_rsq_f32_e32 v101, v101
	v_mul_f32_e32 v100, 0x3fb8aa3b, v100
	v_exp_f32_e32 v104, v100
	v_add_f32_e32 v100, 1.0, v103
	v_rcp_f32_e32 v100, v100
	v_mul_f32_e32 v103, v99, v101
	v_add_f32_e32 v99, -1.0, v106
	v_fma_f32 v99, v99, v81, 1.0
	v_mul_f32_e32 v93, v93, v99
	v_ashrrev_i32_e32 v99, 31, v98
	v_mul_f32_e32 v100, 0xbf1b459e, v100
	v_lshlrev_b64 v[98:99], 9, v[98:99]
	v_mul_f32_e32 v100, 0x3fb8aa3b, v100
	v_or_b32_e32 v98, v98, v31
	v_exp_f32_e32 v102, v100
	v_lshl_add_u64 v[100:101], s[74:75], 0, v[98:99]
	v_cvt_pk_bf16_f32 v89, v89, s0
	global_store_short v[100:101], v89, off
	v_lshl_add_u64 v[100:101], s[76:77], 0, v[98:99]
	v_cvt_pk_bf16_f32 v89, v93, s0
	global_store_short v[100:101], v89, off
	v_lshl_add_u64 v[100:101], s[78:79], 0, v[98:99]
	v_cvt_pk_bf16_f32 v89, v105, s0
	global_store_short v[100:101], v89, off
	v_lshl_add_u64 v[100:101], s[80:81], 0, v[98:99]
	v_cvt_pk_bf16_f32 v89, v103, s0
	global_store_short v[100:101], v89, off
	v_mul_f32_e32 v89, v106, v103
	v_lshl_add_u64 v[100:101], s[82:83], 0, v[98:99]
	v_cvt_pk_bf16_f32 v89, v89, s0
	global_store_short v[100:101], v89, off
	v_lshl_add_u64 v[100:101], s[84:85], 0, v[98:99]
	v_cvt_pk_bf16_f32 v89, v104, s0
	v_sub_f32_e32 v93, v127, v128
	global_store_short v[100:101], v89, off
	v_fma_f32 v93, v93, v2, v128
	v_sub_f32_e32 v100, v129, v128
	v_fmac_f32_e32 v93, v100, v4
	v_mul_f32_e32 v100, v93, v3
	v_mul_f32_e32 v101, v100, v100
	s_nop 1
	v_mov_b32_dpp v101, v101 quad_perm:[1,0,3,2] row_mask:0xf bank_mask:0xf
	v_lshl_add_u64 v[98:99], s[86:87], 0, v[98:99]
	v_cvt_pk_bf16_f32 v89, v102, s0
	global_store_short v[98:99], v89, off
	v_sub_f32_e32 v89, v136, v140
	s_waitcnt lgkmcnt(0)
	v_fmac_f32_e32 v101, v100, v100
	s_nop 1
	v_fma_f32 v89, v89, v112, v140
	v_sub_f32_e32 v98, v144, v140
	v_fmac_f32_e32 v89, v98, v110
	v_sub_f32_e32 v98, v138, v87
	s_waitcnt lgkmcnt(0)
	v_add_f32_dpp v99, v101, v101 quad_perm:[2,3,0,1] row_mask:0xf bank_mask:0xf
	s_nop 1
	v_fma_f32 v102, v98, v108, v87
	v_sub_f32_e32 v98, v85, v87
	v_fmac_f32_e32 v102, v98, v5
	v_mul_f32_e32 v16, 0xbfb8aa3b, v16
	s_waitcnt lgkmcnt(0)
	v_add_f32_dpp v99, v99, v99 row_half_mirror row_mask:0xf bank_mask:0xf
	s_nop 1
	v_exp_f32_e32 v16, v16
	v_mul_f32_e32 v13, 0xbfb8aa3b, v13
	v_exp_f32_e32 v13, v13
	v_mul_f32_e32 v15, 0xbfb8aa3b, v15
	s_waitcnt lgkmcnt(0)
	v_add_f32_dpp v98, v99, v99 row_mirror row_mask:0xf bank_mask:0xf
	v_mov_b32_e32 v99, v98
	s_nop 1
	v_permlane16_swap_b32_e32 v99, v98
	v_add_f32_e32 v16, 1.0, v16
	v_rcp_f32_e32 v16, v16
	v_exp_f32_e32 v15, v15
	v_add_f32_e32 v13, 1.0, v13
	s_waitcnt lgkmcnt(0)
	v_add_f32_e32 v98, v98, v99
	v_mov_b32_e32 v99, v98
	s_nop 1
	v_permlane32_swap_b32_e32 v99, v98
	v_rcp_f32_e32 v13, v13
	v_add_f32_e32 v15, 1.0, v15
	v_rcp_f32_e32 v15, v15
	v_cvt_pk_bf16_f32 v89, v89, s0
	s_waitcnt lgkmcnt(0)
	v_add_f32_e32 v98, v98, v99
	v_add_f32_e32 v98, 0x2b8cbccc, v98
	v_rsq_f32_e32 v98, v98
	v_mul_f32_e32 v13, 0xbf1b459e, v13
	v_mul_f32_e32 v13, 0x3fb8aa3b, v13
	v_mul_f32_e32 v15, 0xbf1b459e, v15
	v_mul_f32_e32 v100, v100, v98
	v_add_f32_e32 v98, -1.0, v16
	v_fma_f32 v98, v98, v81, 1.0
	v_mul_f32_e32 v101, v93, v98
	v_ashrrev_i32_e32 v93, 31, v92
	v_lshlrev_b64 v[92:93], 9, v[92:93]
	v_or_b32_e32 v92, v92, v31
	v_lshl_add_u64 v[98:99], s[74:75], 0, v[92:93]
	v_exp_f32_e32 v13, v13
	v_mul_f32_e32 v15, 0x3fb8aa3b, v15
	global_store_short v[98:99], v89, off
	v_lshl_add_u64 v[98:99], s[76:77], 0, v[92:93]
	v_cvt_pk_bf16_f32 v89, v101, s0
	v_exp_f32_e32 v15, v15
	global_store_short v[98:99], v89, off
	v_lshl_add_u64 v[98:99], s[78:79], 0, v[92:93]
	v_cvt_pk_bf16_f32 v89, v102, s0
	global_store_short v[98:99], v89, off
	v_lshl_add_u64 v[98:99], s[80:81], 0, v[92:93]
	v_cvt_pk_bf16_f32 v89, v100, s0
	v_mul_f32_e32 v16, v16, v100
	global_store_short v[98:99], v89, off
	v_lshl_add_u64 v[98:99], s[82:83], 0, v[92:93]
	v_cvt_pk_bf16_f32 v16, v16, s0
	global_store_short v[98:99], v16, off
	v_lshl_add_u64 v[98:99], s[84:85], 0, v[92:93]
	v_cvt_pk_bf16_f32 v13, v13, s0
	global_store_short v[98:99], v13, off
	v_cvt_pk_bf16_f32 v13, v15, s0
	v_sub_f32_e32 v15, v128, v129
	v_fma_f32 v15, v15, v2, v129
	v_sub_f32_e32 v16, v130, v129
	v_fmac_f32_e32 v15, v16, v4
	v_mul_f32_e32 v16, v15, v3
	v_mul_f32_e32 v89, v16, v16
	s_nop 1
	v_mov_b32_dpp v89, v89 quad_perm:[1,0,3,2] row_mask:0xf bank_mask:0xf
	v_lshl_add_u64 v[92:93], s[86:87], 0, v[92:93]
	global_store_short v[92:93], v13, off
	v_sub_f32_e32 v13, v140, v144
	v_fma_f32 v92, v13, v112, v144
	s_waitcnt lgkmcnt(0)
	v_fmac_f32_e32 v89, v16, v16
	s_nop 1
	v_sub_f32_e32 v13, v145, v144
	v_fmac_f32_e32 v92, v13, v110
	v_sub_f32_e32 v13, v87, v85
	v_mul_f32_e32 v17, 0xbfb8aa3b, v17
	s_waitcnt lgkmcnt(0)
	v_add_f32_dpp v87, v89, v89 quad_perm:[2,3,0,1] row_mask:0xf bank_mask:0xf
	s_nop 1
	v_exp_f32_e32 v17, v17
	v_mul_f32_e32 v12, 0xbfb8aa3b, v12
	v_exp_f32_e32 v12, v12
	v_fma_f32 v98, v13, v108, v85
	s_waitcnt lgkmcnt(0)
	v_add_f32_dpp v87, v87, v87 row_half_mirror row_mask:0xf bank_mask:0xf
	s_nop 1
	v_sub_f32_e32 v13, v146, v85
	v_fmac_f32_e32 v98, v13, v5
	v_add_f32_e32 v13, 1.0, v17
	v_add_f32_e32 v12, 1.0, v12
	s_waitcnt lgkmcnt(0)
	v_add_f32_dpp v17, v87, v87 row_mirror row_mask:0xf bank_mask:0xf
	v_mov_b32_e32 v87, v17
	s_nop 1
	v_permlane16_swap_b32_e32 v87, v17
	v_rcp_f32_e32 v12, v12
	v_rcp_f32_e32 v89, v13
	v_mul_f32_e32 v13, 0xbfb8aa3b, v14
	v_exp_f32_e32 v13, v13
	s_waitcnt lgkmcnt(0)
	v_add_f32_e32 v14, v17, v87
	v_mul_f32_e32 v12, 0xbf1b459e, v12
	v_mov_b32_e32 v17, v14
	s_nop 1
	v_permlane32_swap_b32_e32 v17, v14
	v_mul_f32_e32 v12, 0x3fb8aa3b, v12
	v_exp_f32_e32 v93, v12
	v_add_f32_e32 v12, 1.0, v13
	v_rcp_f32_e32 v12, v12
	s_waitcnt lgkmcnt(0)
	v_add_f32_e32 v13, v14, v17
	v_add_f32_e32 v13, 0x2b8cbccc, v13
	v_rsq_f32_e32 v13, v13
	v_mul_f32_e32 v12, 0xbf1b459e, v12
	v_mul_f32_e32 v12, 0x3fb8aa3b, v12
	v_exp_f32_e32 v17, v12
	v_add_f32_e32 v12, -1.0, v89
	v_fma_f32 v12, v12, v81, 1.0
	v_ashrrev_i32_e32 v87, 31, v86
	v_mul_f32_e32 v16, v16, v13
	v_mul_f32_e32 v99, v15, v12
	v_lshlrev_b64 v[12:13], 9, v[86:87]
	v_or_b32_e32 v12, v12, v31
	v_lshl_add_u64 v[14:15], s[74:75], 0, v[12:13]
	v_cvt_pk_bf16_f32 v86, v92, s0
	global_store_short v[14:15], v86, off
	v_lshl_add_u64 v[14:15], s[76:77], 0, v[12:13]
	v_cvt_pk_bf16_f32 v86, v99, s0
	global_store_short v[14:15], v86, off
	v_lshl_add_u64 v[14:15], s[78:79], 0, v[12:13]
	v_cvt_pk_bf16_f32 v86, v98, s0
	global_store_short v[14:15], v86, off
	v_lshl_add_u64 v[14:15], s[80:81], 0, v[12:13]
	v_cvt_pk_bf16_f32 v86, v16, s0
	v_mul_f32_e32 v16, v89, v16
	global_store_short v[14:15], v86, off
	v_lshl_add_u64 v[14:15], s[82:83], 0, v[12:13]
	v_cvt_pk_bf16_f32 v16, v16, s0
	global_store_short v[14:15], v16, off
	v_lshl_add_u64 v[14:15], s[84:85], 0, v[12:13]
	v_cvt_pk_bf16_f32 v16, v93, s0
	global_store_short v[14:15], v16, off
	v_sub_f32_e32 v15, v129, v130
	v_fma_f32 v15, v15, v2, v130
	v_sub_f32_e32 v16, v83, v130
	v_fmac_f32_e32 v15, v16, v4
	v_mul_f32_e32 v16, v15, v3
	v_cvt_pk_bf16_f32 v14, v17, s0
	v_mul_f32_e32 v17, v16, v16
	s_nop 1
	v_mov_b32_dpp v17, v17 quad_perm:[1,0,3,2] row_mask:0xf bank_mask:0xf
	v_lshl_add_u64 v[12:13], s[86:87], 0, v[12:13]
	global_store_short v[12:13], v14, off
	v_sub_f32_e32 v12, v144, v145
	v_fma_f32 v86, v12, v112, v145
	s_waitcnt lgkmcnt(0)
	v_fmac_f32_e32 v17, v16, v16
	s_nop 1
	v_sub_f32_e32 v12, v147, v145
	v_fmac_f32_e32 v86, v12, v110
	v_sub_f32_e32 v12, v85, v146
	v_fma_f32 v85, v12, v108, v146
	s_waitcnt lgkmcnt(0)
	v_add_f32_dpp v13, v17, v17 quad_perm:[2,3,0,1] row_mask:0xf bank_mask:0xf
	s_nop 1
	v_sub_f32_e32 v12, v148, v146
	v_fmac_f32_e32 v85, v12, v5
	v_mul_f32_e32 v10, 0xbfb8aa3b, v10
	v_exp_f32_e32 v10, v10
	s_waitcnt lgkmcnt(0)
	v_add_f32_dpp v13, v13, v13 row_half_mirror row_mask:0xf bank_mask:0xf
	s_nop 1
	v_mul_f32_e32 v8, 0xbfb8aa3b, v8
	v_exp_f32_e32 v8, v8
	v_add_f32_e32 v10, 1.0, v10
	v_rcp_f32_e32 v10, v10
	s_waitcnt lgkmcnt(0)
	v_add_f32_dpp v12, v13, v13 row_mirror row_mask:0xf bank_mask:0xf
	v_mov_b32_e32 v13, v12
	s_nop 1
	v_permlane16_swap_b32_e32 v13, v12
	v_add_f32_e32 v8, 1.0, v8
	v_rcp_f32_e32 v8, v8
	v_ashrrev_i32_e32 v89, 31, v88
	v_mul_f32_e32 v7, 0xbfb8aa3b, v7
	s_waitcnt lgkmcnt(0)
	v_add_f32_e32 v12, v12, v13
	v_mov_b32_e32 v13, v12
	s_nop 1
	v_permlane32_swap_b32_e32 v13, v12
	v_mul_f32_e32 v8, 0xbf1b459e, v8
	v_mul_f32_e32 v8, 0x3fb8aa3b, v8
	v_cvt_pk_bf16_f32 v86, v86, s0
	v_exp_f32_e32 v7, v7
	s_waitcnt lgkmcnt(0)
	v_add_f32_e32 v12, v12, v13
	v_add_f32_e32 v12, 0x2b8cbccc, v12
	v_rsq_f32_e32 v12, v12
	v_exp_f32_e32 v8, v8
	v_add_f32_e32 v7, 1.0, v7
	v_rcp_f32_e32 v7, v7
	v_mul_f32_e32 v16, v16, v12
	v_add_f32_e32 v12, -1.0, v10
	v_fma_f32 v12, v12, v81, 1.0
	v_mul_f32_e32 v17, v15, v12
	v_lshlrev_b64 v[12:13], 9, v[88:89]
	v_or_b32_e32 v12, v12, v31
	v_lshl_add_u64 v[14:15], s[74:75], 0, v[12:13]
	global_store_short v[14:15], v86, off
	v_lshl_add_u64 v[14:15], s[76:77], 0, v[12:13]
	v_cvt_pk_bf16_f32 v17, v17, s0
	global_store_short v[14:15], v17, off
	v_lshl_add_u64 v[14:15], s[78:79], 0, v[12:13]
	v_cvt_pk_bf16_f32 v17, v85, s0
	global_store_short v[14:15], v17, off
	v_lshl_add_u64 v[14:15], s[80:81], 0, v[12:13]
	v_cvt_pk_bf16_f32 v17, v16, s0
	v_mul_f32_e32 v10, v10, v16
	global_store_short v[14:15], v17, off
	v_lshl_add_u64 v[14:15], s[82:83], 0, v[12:13]
	v_cvt_pk_bf16_f32 v10, v10, s0
	global_store_short v[14:15], v10, off
	v_lshl_add_u64 v[14:15], s[84:85], 0, v[12:13]
	v_cvt_pk_bf16_f32 v8, v8, s0
	global_store_short v[14:15], v8, off
	v_sub_f32_e32 v8, v130, v83
	v_fma_f32 v8, v8, v2, v83
	v_sub_f32_e32 v10, v111, v83
	v_fmac_f32_e32 v8, v10, v4
	v_mul_f32_e32 v10, v8, v3
	v_mul_f32_e32 v7, 0xbf1b459e, v7
	v_mul_f32_e32 v14, v10, v10
	v_mul_f32_e32 v7, 0x3fb8aa3b, v7
	s_nop 1
	v_mov_b32_dpp v14, v14 quad_perm:[1,0,3,2] row_mask:0xf bank_mask:0xf
	v_exp_f32_e32 v7, v7
	v_lshl_add_u64 v[12:13], s[86:87], 0, v[12:13]
	v_mul_f32_e32 v11, 0xbfb8aa3b, v11
	v_exp_f32_e32 v11, v11
	v_cvt_pk_bf16_f32 v7, v7, s0
	s_waitcnt lgkmcnt(0)
	v_fmac_f32_e32 v14, v10, v10
	global_store_short v[12:13], v7, off
	s_nop 1
	v_sub_f32_e32 v7, v145, v147
	v_mul_f32_e32 v9, 0xbfb8aa3b, v9
	v_fma_f32 v12, v7, v112, v147
	v_sub_f32_e32 v7, v116, v147
	s_waitcnt lgkmcnt(0)
	v_add_f32_dpp v13, v14, v14 quad_perm:[2,3,0,1] row_mask:0xf bank_mask:0xf
	s_nop 1
	v_exp_f32_e32 v9, v9
	v_fmac_f32_e32 v12, v7, v110
	v_sub_f32_e32 v7, v146, v148
	v_fma_f32 v15, v7, v108, v148
	s_waitcnt lgkmcnt(0)
	v_add_f32_dpp v13, v13, v13 row_half_mirror row_mask:0xf bank_mask:0xf
	s_nop 1
	v_sub_f32_e32 v7, v114, v148
	v_fmac_f32_e32 v15, v7, v5
	v_add_f32_e32 v7, 1.0, v11
	v_add_f32_e32 v9, 1.0, v9
	s_waitcnt lgkmcnt(0)
	v_add_f32_dpp v11, v13, v13 row_mirror row_mask:0xf bank_mask:0xf
	v_mov_b32_e32 v13, v11
	s_nop 1
	v_permlane16_swap_b32_e32 v13, v11
	v_rcp_f32_e32 v9, v9
	v_mul_f32_e32 v6, 0xbfb8aa3b, v6
	v_exp_f32_e32 v6, v6
	v_rcp_f32_e32 v14, v7
	v_mul_f32_e32 v7, 0xbf1b459e, v9
	s_waitcnt lgkmcnt(0)
	v_add_f32_e32 v9, v11, v13
	v_mov_b32_e32 v11, v9
	s_nop 1
	v_permlane32_swap_b32_e32 v11, v9
	v_add_f32_e32 v6, 1.0, v6
	v_rcp_f32_e32 v6, v6
	v_mul_f32_e32 v7, 0x3fb8aa3b, v7
	v_exp_f32_e32 v13, v7
	s_waitcnt lgkmcnt(0)
	v_add_f32_e32 v7, v9, v11
	v_add_f32_e32 v7, 0x2b8cbccc, v7
	v_rsq_f32_e32 v7, v7
	v_mul_f32_e32 v6, 0xbf1b459e, v6
	v_mul_f32_e32 v6, 0x3fb8aa3b, v6
	v_exp_f32_e32 v11, v6
	v_add_f32_e32 v6, -1.0, v14
	v_fma_f32 v6, v6, v81, 1.0
	v_ashrrev_i32_e32 v85, 31, v84
	v_mul_f32_e32 v10, v10, v7
	v_mul_f32_e32 v16, v8, v6
	v_lshlrev_b64 v[6:7], 9, v[84:85]
	v_or_b32_e32 v6, v6, v31
	v_lshl_add_u64 v[8:9], s[74:75], 0, v[6:7]
	v_cvt_pk_bf16_f32 v12, v12, s0
	global_store_short v[8:9], v12, off
	v_lshl_add_u64 v[8:9], s[76:77], 0, v[6:7]
	v_cvt_pk_bf16_f32 v12, v16, s0
	global_store_short v[8:9], v12, off
	v_lshl_add_u64 v[8:9], s[78:79], 0, v[6:7]
	v_cvt_pk_bf16_f32 v12, v15, s0
	global_store_short v[8:9], v12, off
	v_lshl_add_u64 v[8:9], s[80:81], 0, v[6:7]
	v_cvt_pk_bf16_f32 v12, v10, s0
	v_mul_f32_e32 v10, v14, v10
	global_store_short v[8:9], v12, off
	v_lshl_add_u64 v[8:9], s[82:83], 0, v[6:7]
	v_cvt_pk_bf16_f32 v10, v10, s0
	global_store_short v[8:9], v10, off
	v_lshl_add_u64 v[8:9], s[84:85], 0, v[6:7]
	v_cvt_pk_bf16_f32 v10, v13, s0
	global_store_short v[8:9], v10, off
	v_sub_f32_e32 v9, v83, v111
	v_fma_f32 v9, v9, v2, v111
	v_sub_f32_e32 v10, v34, v111
	v_fmac_f32_e32 v9, v10, v4
	v_mul_f32_e32 v10, v9, v3
	v_cvt_pk_bf16_f32 v8, v11, s0
	v_mul_f32_e32 v11, v10, v10
	s_nop 1
	v_mov_b32_dpp v11, v11 quad_perm:[1,0,3,2] row_mask:0xf bank_mask:0xf
	v_lshl_add_u64 v[6:7], s[86:87], 0, v[6:7]
	global_store_short v[6:7], v8, off
	v_mul_f32_e32 v14, 0xbfb8aa3b, v94
	v_sub_f32_e32 v6, v147, v116
	s_waitcnt lgkmcnt(0)
	v_fmac_f32_e32 v11, v10, v10
	s_nop 1
	v_exp_f32_e32 v14, v14
	v_fma_f32 v12, v6, v112, v116
	v_sub_f32_e32 v6, v109, v116
	v_fmac_f32_e32 v12, v6, v110
	s_waitcnt lgkmcnt(0)
	v_add_f32_dpp v7, v11, v11 quad_perm:[2,3,0,1] row_mask:0xf bank_mask:0xf
	s_nop 1
	v_mul_f32_e32 v11, 0xbfb8aa3b, v96
	v_exp_f32_e32 v11, v11
	v_sub_f32_e32 v6, v148, v114
	v_fma_f32 v13, v6, v108, v114
	s_waitcnt lgkmcnt(0)
	v_add_f32_dpp v7, v7, v7 row_half_mirror row_mask:0xf bank_mask:0xf
	s_nop 1
	v_sub_f32_e32 v6, v79, v114
	v_fmac_f32_e32 v13, v6, v5
	v_add_f32_e32 v6, 1.0, v11
	v_add_f32_e32 v11, 1.0, v14
	v_rcp_f32_e32 v11, v11
	s_waitcnt lgkmcnt(0)
	v_add_f32_dpp v7, v7, v7 row_mirror row_mask:0xf bank_mask:0xf
	v_mov_b32_e32 v8, v7
	s_nop 1
	v_permlane16_swap_b32_e32 v8, v7
	v_rcp_f32_e32 v14, v6
	v_mul_f32_e32 v6, 0xbf1b459e, v11
	v_mul_f32_e32 v11, 0xbfb8aa3b, v91
	v_exp_f32_e32 v11, v11
	s_waitcnt lgkmcnt(0)
	v_add_f32_e32 v7, v7, v8
	v_mov_b32_e32 v8, v7
	s_nop 1
	v_permlane32_swap_b32_e32 v8, v7
	v_mul_f32_e32 v6, 0x3fb8aa3b, v6
	v_exp_f32_e32 v15, v6
	v_add_f32_e32 v6, 1.0, v11
	v_rcp_f32_e32 v6, v6
	s_waitcnt lgkmcnt(0)
	v_add_f32_e32 v7, v7, v8
	v_add_f32_e32 v7, 0x2b8cbccc, v7
	v_rsq_f32_e32 v7, v7
	v_mul_f32_e32 v6, 0xbf1b459e, v6
	v_mul_f32_e32 v6, 0x3fb8aa3b, v6
	v_exp_f32_e32 v11, v6
	v_add_f32_e32 v6, -1.0, v14
	v_fma_f32 v6, v6, v81, 1.0
	v_ashrrev_i32_e32 v83, 31, v82
	v_mul_f32_e32 v10, v10, v7
	v_mul_f32_e32 v16, v9, v6
	v_lshlrev_b64 v[6:7], 9, v[82:83]
	v_or_b32_e32 v6, v6, v31
	v_lshl_add_u64 v[8:9], s[74:75], 0, v[6:7]
	v_cvt_pk_bf16_f32 v12, v12, s0
	global_store_short v[8:9], v12, off
	v_lshl_add_u64 v[8:9], s[76:77], 0, v[6:7]
	v_cvt_pk_bf16_f32 v12, v16, s0
	global_store_short v[8:9], v12, off
	v_lshl_add_u64 v[8:9], s[78:79], 0, v[6:7]
	v_cvt_pk_bf16_f32 v12, v13, s0
	global_store_short v[8:9], v12, off
	v_lshl_add_u64 v[8:9], s[80:81], 0, v[6:7]
	v_cvt_pk_bf16_f32 v12, v10, s0
	v_mul_f32_e32 v10, v14, v10
	global_store_short v[8:9], v12, off
	v_lshl_add_u64 v[8:9], s[82:83], 0, v[6:7]
	v_cvt_pk_bf16_f32 v10, v10, s0
	global_store_short v[8:9], v10, off
	v_lshl_add_u64 v[8:9], s[84:85], 0, v[6:7]
	v_cvt_pk_bf16_f32 v10, v15, s0
	global_store_short v[8:9], v10, off
	v_lshl_add_u64 v[6:7], s[86:87], 0, v[6:7]
	v_cvt_pk_bf16_f32 v8, v11, s0
	v_cndmask_b32_e64 v113, 0, v113, s[50:51]
	global_store_short v[6:7], v8, off
	v_sub_f32_e32 v6, v111, v34
	v_sub_f32_e32 v7, v113, v34
	v_fmac_f32_e32 v34, v6, v2
	v_fmac_f32_e32 v34, v7, v4
	v_mul_f32_e32 v2, v34, v3
	v_mul_f32_e32 v3, v2, v2
	s_nop 1
	v_mov_b32_dpp v3, v3 quad_perm:[1,0,3,2] row_mask:0xf bank_mask:0xf
	global_load_dword v122, v[44:45], off
	v_sub_f32_e32 v4, v116, v109
	v_sub_f32_e32 v6, v117, v109
	v_fmac_f32_e32 v109, v4, v112
	s_waitcnt lgkmcnt(0)
	v_fmac_f32_e32 v3, v2, v2
	s_nop 1
	v_fmac_f32_e32 v109, v6, v110
	v_sub_f32_e32 v6, v114, v79
	v_sub_f32_e32 v7, v115, v79
	v_fmac_f32_e32 v79, v6, v108
	s_waitcnt lgkmcnt(0)
	v_add_f32_dpp v3, v3, v3 quad_perm:[2,3,0,1] row_mask:0xf bank_mask:0xf
	s_nop 1
	v_mul_f32_e32 v6, 0xbfb8aa3b, v97
	v_mul_f32_e32 v8, 0xbfb8aa3b, v95
	v_exp_f32_e32 v6, v6
	v_exp_f32_e32 v8, v8
	s_waitcnt lgkmcnt(0)
	v_add_f32_dpp v3, v3, v3 row_half_mirror row_mask:0xf bank_mask:0xf
	s_nop 1
	v_fmac_f32_e32 v79, v7, v5
	v_add_f32_e32 v5, 1.0, v6
	v_add_f32_e32 v6, 1.0, v8
	v_rcp_f32_e32 v6, v6
	s_waitcnt lgkmcnt(0)
	v_add_f32_dpp v3, v3, v3 row_mirror row_mask:0xf bank_mask:0xf
	v_mov_b32_e32 v4, v3
	s_nop 1
	v_permlane16_swap_b32_e32 v4, v3
	v_rcp_f32_e32 v7, v5
	v_mul_f32_e32 v5, 0xbf1b459e, v6
	v_mul_f32_e32 v6, 0xbfb8aa3b, v90
	v_exp_f32_e32 v6, v6
	s_waitcnt lgkmcnt(0)
	v_add_f32_e32 v3, v3, v4
	v_mov_b32_e32 v4, v3
	s_nop 1
	v_permlane32_swap_b32_e32 v4, v3
	v_mul_f32_e32 v5, 0x3fb8aa3b, v5
	v_exp_f32_e32 v8, v5
	v_add_f32_e32 v5, 1.0, v6
	v_rcp_f32_e32 v5, v5
	s_waitcnt lgkmcnt(0)
	v_add_f32_e32 v3, v3, v4
	v_add_f32_e32 v3, 0x2b8cbccc, v3
	v_rsq_f32_e32 v3, v3
	v_mul_f32_e32 v4, 0xbf1b459e, v5
	v_mul_f32_e32 v4, 0x3fb8aa3b, v4
	v_exp_f32_e32 v6, v4
	v_mul_f32_e32 v9, v2, v3
	v_add_f32_e32 v2, -1.0, v7
	v_fma_f32 v2, v2, v81, 1.0
	v_ashrrev_i32_e32 v81, 31, v80
	v_mul_f32_e32 v10, v34, v2
	v_lshlrev_b64 v[2:3], 9, v[80:81]
	v_or_b32_e32 v2, v2, v31
	v_lshl_add_u64 v[4:5], s[74:75], 0, v[2:3]
	v_cvt_pk_bf16_f32 v11, v109, s0
	global_store_short v[4:5], v11, off
	v_lshl_add_u64 v[4:5], s[76:77], 0, v[2:3]
	v_cvt_pk_bf16_f32 v10, v10, s0
	global_store_short v[4:5], v10, off
	v_lshl_add_u64 v[4:5], s[78:79], 0, v[2:3]
	v_cvt_pk_bf16_f32 v10, v79, s0
	global_store_short v[4:5], v10, off
	v_lshl_add_u64 v[4:5], s[80:81], 0, v[2:3]
	v_cvt_pk_bf16_f32 v10, v9, s0
	v_mul_f32_e32 v7, v7, v9
	global_store_short v[4:5], v10, off
	v_lshl_add_u64 v[4:5], s[82:83], 0, v[2:3]
	v_cvt_pk_bf16_f32 v7, v7, s0
	global_store_short v[4:5], v7, off
	v_lshl_add_u64 v[4:5], s[84:85], 0, v[2:3]
	v_cvt_pk_bf16_f32 v7, v8, s0
	global_store_short v[4:5], v7, off
	v_lshl_add_u64 v[2:3], s[86:87], 0, v[2:3]
	v_cvt_pk_bf16_f32 v4, v6, s0
	global_store_short v[2:3], v4, off
	ds_read2st64_b32 v[116:117], v141 offset1:2
	ds_read_b128 v[2:5], v142 offset:384
	ds_read2st64_b32 v[118:119], v141 offset0:4 offset1:6
	ds_read_b128 v[6:9], v142 offset:400
	ds_read_b128 v[10:13], v142 offset:416
	ds_read_b128 v[14:17], v142 offset:432
	ds_read_b128 v[80:83], v142 offset:896
	s_waitcnt lgkmcnt(5)
	v_mul_f32_e32 v3, v117, v3
	v_fmac_f32_e32 v3, v116, v2
	s_waitcnt lgkmcnt(4)
	v_mul_f32_e32 v2, v119, v5
	v_fmac_f32_e32 v2, v118, v4
	ds_read_b128 v[84:87], v142 offset:1408
	v_add_f32_e32 v2, v3, v2
	ds_read_b128 v[88:91], v142 offset:1920
	ds_read_b128 v[92:95], v142 offset:2432
	ds_read_b128 v[96:99], v142 offset:2944
	s_waitcnt vmcnt(7)
	v_add_f32_e32 v34, v122, v2
	ds_read_b128 v[2:5], v142 offset:912
	s_waitcnt lgkmcnt(5)
	v_mul_f32_e32 v79, v117, v81
	v_fmac_f32_e32 v79, v116, v80
	v_mul_f32_e32 v80, v119, v83
	v_fmac_f32_e32 v80, v118, v82
	v_add_f32_e32 v79, v79, v80
	ds_read_b128 v[80:83], v142 offset:1424
	s_waitcnt lgkmcnt(5)
	v_mul_f32_e32 v85, v117, v85
	v_fmac_f32_e32 v85, v116, v84
	v_mul_f32_e32 v84, v119, v87
	v_fmac_f32_e32 v84, v118, v86
	v_add_f32_e32 v84, v85, v84
	v_add_f32_e32 v120, v122, v84
	ds_read_b128 v[84:87], v142 offset:1936
	s_waitcnt lgkmcnt(5)
	v_mul_f32_e32 v89, v117, v89
	v_fmac_f32_e32 v89, v116, v88
	v_mul_f32_e32 v88, v119, v91
	v_fmac_f32_e32 v88, v118, v90
	v_add_f32_e32 v88, v89, v88
	v_add_f32_e32 v121, v122, v88
	ds_read_b128 v[88:91], v142 offset:2448
	s_waitcnt lgkmcnt(5)
	v_mul_f32_e32 v93, v117, v93
	v_fmac_f32_e32 v93, v116, v92
	v_mul_f32_e32 v92, v119, v95
	v_fmac_f32_e32 v92, v118, v94
	v_add_f32_e32 v92, v93, v92
	ds_read_b128 v[100:103], v142 offset:3456
	v_add_f32_e32 v123, v122, v92
	ds_read_b128 v[92:95], v142 offset:2960
	s_waitcnt lgkmcnt(6)
	v_mul_f32_e32 v97, v117, v97
	v_fmac_f32_e32 v97, v116, v96
	v_mul_f32_e32 v96, v119, v99
	v_fmac_f32_e32 v96, v118, v98
	v_add_f32_e32 v96, v97, v96
	v_add_f32_e32 v124, v122, v96
	ds_read_b128 v[96:99], v142 offset:3472
	s_waitcnt lgkmcnt(2)
	v_mul_f32_e32 v101, v117, v101
	v_fmac_f32_e32 v101, v116, v100
	v_mul_f32_e32 v100, v119, v103
	v_fmac_f32_e32 v100, v118, v102
	v_add_f32_e32 v104, v101, v100
	ds_read_b128 v[100:103], v143 offset:384
	v_add_f32_e32 v125, v122, v104
	ds_read_b128 v[104:107], v143 offset:400
	ds_read_b128 v[108:111], v143 offset:416
	ds_read_b128 v[112:115], v143 offset:432
	v_add_f32_e32 v79, v122, v79
	s_mov_b32 s2, 0xbfb8aa3b
	s_waitcnt lgkmcnt(3)
	v_mul_f32_e32 v117, v117, v101
	v_fmac_f32_e32 v117, v116, v100
	v_mul_f32_e32 v116, v119, v103
	ds_read2st64_b32 v[100:101], v141 offset0:8 offset1:10
	v_fmac_f32_e32 v116, v118, v102
	ds_read2st64_b32 v[102:103], v141 offset0:12 offset1:14
	v_add_f32_e32 v116, v117, v116
	v_add_f32_e32 v116, v122, v116
	s_waitcnt lgkmcnt(1)
	v_mul_f32_e32 v7, v101, v7
	v_mul_f32_e32 v3, v101, v3
	v_fmac_f32_e32 v7, v100, v6
	s_waitcnt lgkmcnt(0)
	v_mul_f32_e32 v6, v103, v9
	v_fmac_f32_e32 v3, v100, v2
	v_mul_f32_e32 v2, v103, v5
	v_fmac_f32_e32 v6, v102, v8
	v_fmac_f32_e32 v2, v102, v4
	v_add_f32_e32 v6, v7, v6
	v_add_f32_e32 v2, v3, v2
	v_add_f32_e32 v6, v34, v6
	v_add_f32_e32 v34, v79, v2
	v_mul_f32_e32 v2, v101, v81
	v_mul_f32_e32 v3, v103, v83
	v_fmac_f32_e32 v2, v100, v80
	v_fmac_f32_e32 v3, v102, v82
	v_add_f32_e32 v2, v2, v3
	v_add_f32_e32 v79, v120, v2
	v_mul_f32_e32 v2, v101, v85
	v_mul_f32_e32 v3, v103, v87
	v_fmac_f32_e32 v2, v100, v84
	v_fmac_f32_e32 v3, v102, v86
	v_add_f32_e32 v2, v2, v3
	v_add_f32_e32 v117, v121, v2
	v_mul_f32_e32 v2, v101, v89
	v_mul_f32_e32 v3, v103, v91
	v_fmac_f32_e32 v2, v100, v88
	v_fmac_f32_e32 v3, v102, v90
	v_add_f32_e32 v2, v2, v3
	v_add_f32_e32 v118, v123, v2
	v_mul_f32_e32 v2, v101, v93
	v_mul_f32_e32 v3, v103, v95
	v_fmac_f32_e32 v2, v100, v92
	v_fmac_f32_e32 v3, v102, v94
	v_add_f32_e32 v2, v2, v3
	v_add_f32_e32 v119, v124, v2
	v_mul_f32_e32 v2, v101, v97
	v_mul_f32_e32 v3, v103, v99
	v_fmac_f32_e32 v2, v100, v96
	v_fmac_f32_e32 v3, v102, v98
	v_add_f32_e32 v2, v2, v3
	ds_read2st64_b32 v[96:97], v141 offset0:16 offset1:18
	ds_read2st64_b32 v[98:99], v141 offset0:20 offset1:22
	v_add_f32_e32 v120, v125, v2
	v_mul_f32_e32 v2, v101, v105
	v_mul_f32_e32 v3, v103, v107
	v_fmac_f32_e32 v2, v100, v104
	v_fmac_f32_e32 v3, v102, v106
	v_add_f32_e32 v2, v2, v3
	v_add_f32_e32 v100, v116, v2
	ds_read_b128 v[2:5], v142 offset:928
	s_waitcnt lgkmcnt(2)
	v_mul_f32_e32 v7, v97, v11
	s_waitcnt lgkmcnt(1)
	v_mul_f32_e32 v8, v99, v13
	v_fmac_f32_e32 v7, v96, v10
	v_fmac_f32_e32 v8, v98, v12
	v_add_f32_e32 v7, v7, v8
	v_add_f32_e32 v101, v6, v7
	ds_read_b128 v[6:9], v142 offset:1440
	ds_read_b128 v[10:13], v142 offset:944
	s_waitcnt lgkmcnt(2)
	v_mul_f32_e32 v3, v97, v3
	v_fmac_f32_e32 v3, v96, v2
	v_mul_f32_e32 v2, v99, v5
	v_fmac_f32_e32 v2, v98, v4
	v_add_f32_e32 v2, v3, v2
	v_add_f32_e32 v34, v34, v2
	ds_read_b128 v[2:5], v142 offset:1456
	s_waitcnt lgkmcnt(2)
	v_mul_f32_e32 v7, v97, v7
	ds_read_b128 v[80:83], v142 offset:1952
	ds_read_b128 v[84:87], v142 offset:1968
	v_fmac_f32_e32 v7, v96, v6
	v_mul_f32_e32 v6, v99, v9
	v_fmac_f32_e32 v6, v98, v8
	v_add_f32_e32 v6, v7, v6
	v_add_f32_e32 v79, v79, v6
	ds_read_b128 v[6:9], v142 offset:2464
	s_waitcnt lgkmcnt(2)
	v_mul_f32_e32 v81, v97, v81
	v_fmac_f32_e32 v81, v96, v80
	v_mul_f32_e32 v80, v99, v83
	v_fmac_f32_e32 v80, v98, v82
	v_add_f32_e32 v80, v81, v80
	v_add_f32_e32 v102, v117, v80
	ds_read_b128 v[80:83], v142 offset:2480
	s_waitcnt lgkmcnt(1)
	v_mul_f32_e32 v7, v97, v7
	ds_read_b128 v[88:91], v142 offset:2976
	ds_read_b128 v[92:95], v142 offset:2992
	v_fmac_f32_e32 v7, v96, v6
	v_mul_f32_e32 v6, v99, v9
	v_fmac_f32_e32 v6, v98, v8
	v_add_f32_e32 v6, v7, v6
	v_add_f32_e32 v103, v118, v6
	ds_read_b128 v[6:9], v142 offset:3488
	s_waitcnt lgkmcnt(2)
	v_mul_f32_e32 v89, v97, v89
	v_fmac_f32_e32 v89, v96, v88
	v_mul_f32_e32 v88, v99, v91
	v_fmac_f32_e32 v88, v98, v90
	v_add_f32_e32 v88, v89, v88
	v_add_f32_e32 v104, v119, v88
	ds_read_b128 v[88:91], v142 offset:3504
	s_waitcnt lgkmcnt(1)
	v_mul_f32_e32 v7, v97, v7
	v_fmac_f32_e32 v7, v96, v6
	v_mul_f32_e32 v6, v99, v9
	v_fmac_f32_e32 v6, v98, v8
	v_add_f32_e32 v6, v7, v6
	v_add_f32_e32 v105, v120, v6
	v_mul_f32_e32 v6, v97, v109
	v_mul_f32_e32 v7, v99, v111
	v_fmac_f32_e32 v6, v96, v108
	ds_read2st64_b32 v[96:97], v141 offset0:24 offset1:26
	v_fmac_f32_e32 v7, v98, v110
	ds_read2st64_b32 v[98:99], v141 offset0:28 offset1:30
	v_add_f32_e32 v6, v6, v7
	v_add_f32_e32 v100, v100, v6
	s_waitcnt lgkmcnt(1)
	v_mul_f32_e32 v6, v97, v15
	v_fmac_f32_e32 v6, v96, v14
	s_waitcnt lgkmcnt(0)
	v_mul_f32_e32 v7, v99, v17
	v_fmac_f32_e32 v7, v98, v16
	v_mul_f32_e32 v3, v97, v3
	v_add_f32_e32 v6, v6, v7
	v_fmac_f32_e32 v3, v96, v2
	v_mul_f32_e32 v2, v99, v5
	v_add_f32_e32 v9, v101, v6
	v_mul_f32_e32 v6, v97, v11
	v_mul_f32_e32 v7, v99, v13
	v_fmac_f32_e32 v2, v98, v4
	v_fmac_f32_e32 v6, v96, v10
	v_fmac_f32_e32 v7, v98, v12
	v_add_f32_e32 v2, v3, v2
	v_add_f32_e32 v6, v6, v7
	v_add_f32_e32 v7, v79, v2
	v_mul_f32_e32 v2, v97, v85
	v_mul_f32_e32 v3, v99, v87
	v_fmac_f32_e32 v2, v96, v84
	v_fmac_f32_e32 v3, v98, v86
	v_add_f32_e32 v2, v2, v3
	v_add_f32_e32 v8, v34, v6
	v_add_f32_e32 v6, v102, v2
	v_mul_f32_e32 v2, v97, v81
	v_mul_f32_e32 v3, v99, v83
	v_fmac_f32_e32 v2, v96, v80
	v_fmac_f32_e32 v3, v98, v82
	v_add_f32_e32 v2, v2, v3
	v_add_f32_e32 v5, v103, v2
	v_mul_f32_e32 v2, v97, v93
	v_mul_f32_e32 v3, v99, v95
	v_fmac_f32_e32 v2, v96, v92
	v_fmac_f32_e32 v3, v98, v94
	v_add_f32_e32 v2, v2, v3
	v_mul_f32_e64 v11, |v9|, s2
	v_add_f32_e32 v3, v104, v2
	v_mul_f32_e32 v2, v97, v89
	v_mul_f32_e32 v4, v99, v91
	v_exp_f32_e32 v11, v11
	v_fmac_f32_e32 v2, v96, v88
	v_fmac_f32_e32 v4, v98, v90
	v_add_f32_e32 v2, v2, v4
	v_mul_f32_e32 v4, v97, v113
	v_mul_f32_e32 v10, v99, v115
	v_fmac_f32_e32 v4, v96, v112
	v_fmac_f32_e32 v10, v98, v114
	v_add_f32_e32 v4, v4, v10
	v_add_f32_e32 v10, 1.0, v11
	v_log_f32_e32 v10, v10
	v_max_f32_e64 v9, -v9, 0
	s_ashr_i32 s89, s88, 31
	v_lshl_add_u64 v[12:13], v[46:47], 0, s[88:89]
	v_fmac_f32_e32 v9, 0x3f317218, v10
	v_mul_f32_e64 v10, |v8|, s2
	v_exp_f32_e32 v14, v10
	v_lshlrev_b64 v[10:11], 9, v[12:13]
	v_add_f32_e32 v4, v100, v4
	v_mul_f32_e32 v9, 0xbd800000, v9
	v_lshl_add_u64 v[100:101], v[48:49], 0, v[10:11]
	global_store_dword v[100:101], v9, off
	v_add_f32_e32 v9, 1.0, v14
	v_log_f32_e32 v9, v9
	v_mul_f32_e64 v10, |v7|, s2
	v_exp_f32_e32 v10, v10
	v_max_f32_e64 v8, -v8, 0
	v_fmac_f32_e32 v8, 0x3f317218, v9
	v_mul_f32_e32 v8, 0xbd800000, v8
	global_store_dword v[100:101], v8, off offset:512
	v_add_f32_e32 v8, 1.0, v10
	v_log_f32_e32 v8, v8
	v_mul_f32_e64 v9, |v6|, s2
	v_exp_f32_e32 v9, v9
	v_max_f32_e64 v7, -v7, 0
	v_fmac_f32_e32 v7, 0x3f317218, v8
	v_mul_f32_e32 v7, 0xbd800000, v7
	global_store_dword v[100:101], v7, off offset:1024
	v_add_f32_e32 v7, 1.0, v9
	v_log_f32_e32 v7, v7
	v_mul_f32_e64 v8, |v5|, s2
	v_exp_f32_e32 v8, v8
	v_max_f32_e64 v6, -v6, 0
	v_fmac_f32_e32 v6, 0x3f317218, v7
	v_mul_f32_e32 v6, 0xbd800000, v6
	global_store_dword v[100:101], v6, off offset:1536
	v_add_f32_e32 v6, 1.0, v8
	v_log_f32_e32 v6, v6
	v_mul_f32_e64 v7, |v3|, s2
	v_exp_f32_e32 v7, v7
	v_max_f32_e64 v5, -v5, 0
	v_fmac_f32_e32 v5, 0x3f317218, v6
	v_add_f32_e32 v2, v105, v2
	v_mul_f32_e32 v5, 0xbd800000, v5
	global_store_dword v[100:101], v5, off offset:2048
	v_add_f32_e32 v5, 1.0, v7
	v_mul_f32_e64 v6, |v2|, s2
	v_log_f32_e32 v5, v5
	v_exp_f32_e32 v6, v6
	v_max_f32_e64 v3, -v3, 0
	s_add_i32 s4, s88, -2
	v_fmac_f32_e32 v3, 0x3f317218, v5
	v_add_f32_e32 v5, 1.0, v6
	v_mul_f32_e64 v6, |v4|, s2
	v_exp_f32_e32 v6, v6
	v_log_f32_e32 v5, v5
	v_mul_f32_e32 v3, 0xbd800000, v3
	v_mad_i64_i32 v[102:103], s[2:3], s88, v202, v[76:77]
	s_cmp_ge_i32 s4, s1
	global_store_dword v[100:101], v3, off offset:2560
	v_add_f32_e32 v3, 1.0, v6
	s_cselect_b64 s[2:3], -1, 0
	s_cmp_lt_i32 s4, s0
	v_max_f32_e64 v2, -v2, 0
	v_log_f32_e32 v3, v3
	s_cselect_b64 s[4:5], -1, 0
	v_fmac_f32_e32 v2, 0x3f317218, v5
	s_and_b64 vcc, s[2:3], s[4:5]
	v_mul_f32_e32 v2, 0xbd800000, v2
	s_and_b64 s[2:3], vcc, exec
	global_store_dword v[100:101], v2, off offset:3072
	v_max_f32_e64 v2, -v4, 0
	s_cselect_b32 s3, -1, 0
	s_cselect_b32 s2, 0xffffcc00, 0
	s_add_i32 s4, s88, -1
	v_fmac_f32_e32 v2, 0x3f317218, v3
	s_cmp_ge_i32 s4, s1
	v_mul_f32_e32 v34, 0xbd800000, v2
	v_lshl_add_u64 v[2:3], v[102:103], 0, s[2:3]
	s_cselect_b64 s[2:3], -1, 0
	s_cmp_lt_i32 s4, s0
	s_cselect_b64 s[4:5], -1, 0
	s_and_b64 s[2:3], s[2:3], s[4:5]
	s_and_b64 s[4:5], s[2:3], exec
	s_cselect_b32 s5, -1, 0
	s_cselect_b32 s4, 0xffffe600, 0
	s_cmp_ge_i32 s88, s1
	v_lshl_add_u64 v[4:5], v[102:103], 0, s[4:5]
	s_cselect_b64 s[4:5], -1, 0
	s_cmp_lt_i32 s88, s0
	s_cselect_b64 s[6:7], -1, 0
	s_and_b64 s[4:5], s[4:5], s[6:7]
	s_or_b32 s10, s88, 1
	s_cmp_ge_i32 s10, s1
	s_cselect_b64 s[6:7], -1, 0
	s_cmp_lt_i32 s10, s0
	s_cselect_b64 s[8:9], -1, 0
	s_and_b64 s[40:41], s[6:7], s[8:9]
	s_and_b64 s[6:7], s[40:41], exec
	s_cselect_b32 s6, 0x1a00, 0
	s_mov_b32 s72, 0
	s_or_b32 s14, s88, 2
	s_mov_b32 s73, 1
	s_mov_b32 s7, s72
	s_cmp_ge_i32 s14, s1
	v_lshl_add_u64 v[6:7], v[102:103], 0, s[6:7]
	s_cselect_b64 s[6:7], -1, 0
	s_cmp_lt_i32 s14, s0
	s_cselect_b64 s[8:9], -1, 0
	s_and_b64 s[42:43], s[6:7], s[8:9]
	s_and_b64 s[6:7], s[42:43], exec
	s_cselect_b32 s6, 0x3400, 0
	s_mov_b32 s7, s72
	v_lshl_add_u64 v[8:9], v[102:103], 0, s[6:7]
	s_or_b32 s6, s88, 3
	s_cmp_ge_i32 s6, s1
	s_cselect_b64 s[8:9], -1, 0
	s_cmp_lt_i32 s6, s0
	s_cselect_b64 s[18:19], -1, 0
	s_and_b64 s[44:45], s[8:9], s[18:19]
	s_and_b64 s[8:9], s[44:45], exec
	s_cselect_b32 s8, 0x4e00, 0
	s_mov_b32 s9, s72
	v_lshl_add_u64 v[10:11], v[102:103], 0, s[8:9]
	s_or_b32 s8, s88, 4
	s_cmp_ge_i32 s8, s1
	s_cselect_b64 s[18:19], -1, 0
	s_cmp_lt_i32 s8, s0
	s_cselect_b64 s[22:23], -1, 0
	s_and_b64 s[46:47], s[18:19], s[22:23]
	s_and_b64 s[18:19], s[46:47], exec
	s_cselect_b32 s18, 0x6800, 0
	s_or_b32 s34, s88, 5
	s_mov_b32 s19, s72
	s_cmp_ge_i32 s34, s1
	v_lshl_add_u64 v[12:13], v[102:103], 0, s[18:19]
	s_cselect_b64 s[18:19], -1, 0
	s_cmp_lt_i32 s34, s0
	s_cselect_b64 s[22:23], -1, 0
	s_and_b64 s[48:49], s[18:19], s[22:23]
	s_and_b64 s[18:19], s[48:49], exec
	s_cselect_b32 s18, 0x8200, 0
	s_or_b32 s36, s88, 6
	s_mov_b32 s19, s72
	s_cmp_ge_i32 s36, s1
	v_lshl_add_u64 v[14:15], v[102:103], 0, s[18:19]
	s_cselect_b64 s[18:19], -1, 0
	s_cmp_lt_i32 s36, s0
	s_cselect_b64 s[22:23], -1, 0
	s_and_b64 s[50:51], s[18:19], s[22:23]
	s_and_b64 s[18:19], s[50:51], exec
	s_cselect_b32 s18, 0x9c00, 0
	s_or_b32 s28, s88, 7
	s_mov_b32 s19, s72
	s_cmp_ge_i32 s28, s1
	v_lshl_add_u64 v[16:17], v[102:103], 0, s[18:19]
	s_cselect_b64 s[18:19], -1, 0
	s_cmp_lt_i32 s28, s0
	s_cselect_b64 s[22:23], -1, 0
	s_and_b64 s[52:53], s[18:19], s[22:23]
	s_and_b64 s[18:19], s[52:53], exec
	s_cselect_b32 s18, 0xb600, 0
	s_or_b32 s30, s88, 8
	s_mov_b32 s19, s72
	s_cmp_ge_i32 s30, s1
	v_lshl_add_u64 v[80:81], v[102:103], 0, s[18:19]
	s_cselect_b64 s[18:19], -1, 0
	s_cmp_lt_i32 s30, s0
	s_cselect_b64 s[22:23], -1, 0
	s_and_b64 s[54:55], s[18:19], s[22:23]
	s_and_b64 s[18:19], s[54:55], exec
	s_cselect_b32 s18, 0xd000, 0
	s_or_b32 s24, s88, 9
	s_mov_b32 s19, s72
	s_cmp_ge_i32 s24, s1
	v_lshl_add_u64 v[82:83], v[102:103], 0, s[18:19]
	s_cselect_b64 s[18:19], -1, 0
	s_cmp_lt_i32 s24, s0
	s_cselect_b64 s[22:23], -1, 0
	s_and_b64 s[56:57], s[18:19], s[22:23]
	s_and_b64 s[18:19], s[56:57], exec
	s_cselect_b32 s18, 0xea00, 0
	s_or_b32 s26, s88, 10
	s_mov_b32 s19, s72
	s_cmp_ge_i32 s26, s1
	v_lshl_add_u64 v[84:85], v[102:103], 0, s[18:19]
	s_cselect_b64 s[18:19], -1, 0
	s_cmp_lt_i32 s26, s0
	s_cselect_b64 s[22:23], -1, 0
	s_and_b64 s[58:59], s[18:19], s[22:23]
	s_and_b64 s[18:19], s[58:59], exec
	s_cselect_b32 s18, 0x10400, 0
	s_mov_b32 s19, s72
	v_lshl_add_u64 v[86:87], v[102:103], 0, s[18:19]
	s_or_b32 s18, s88, 11
	s_cmp_ge_i32 s18, s1
	s_cselect_b64 s[22:23], -1, 0
	s_cmp_lt_i32 s18, s0
	s_cselect_b64 s[60:61], -1, 0
	s_and_b64 s[60:61], s[22:23], s[60:61]
	s_and_b64 s[22:23], s[60:61], exec
	s_cselect_b32 s22, 0x11e00, 0
	s_mov_b32 s23, s72
	v_lshl_add_u64 v[88:89], v[102:103], 0, s[22:23]
	s_or_b32 s22, s88, 12
	s_cmp_ge_i32 s22, s1
	s_cselect_b64 s[62:63], -1, 0
	s_cmp_lt_i32 s22, s0
	s_cselect_b64 s[64:65], -1, 0
	s_and_b64 s[62:63], s[62:63], s[64:65]
	s_and_b64 s[64:65], s[62:63], exec
	s_cselect_b32 s64, 0x13800, 0
	s_or_b32 s92, s88, 13
	s_mov_b32 s65, s72
	s_cmp_ge_i32 s92, s1
	v_lshl_add_u64 v[90:91], v[102:103], 0, s[64:65]
	s_cselect_b64 s[64:65], -1, 0
	s_cmp_lt_i32 s92, s0
	s_cselect_b64 s[66:67], -1, 0
	s_and_b64 s[64:65], s[64:65], s[66:67]
	s_and_b64 s[66:67], s[64:65], exec
	s_cselect_b32 s66, 0x15200, 0
	s_or_b32 s94, s88, 14
	s_mov_b32 s67, s72
	s_cmp_ge_i32 s94, s1
	v_lshl_add_u64 v[92:93], v[102:103], 0, s[66:67]
	s_cselect_b64 s[66:67], -1, 0
	s_cmp_lt_i32 s94, s0
	s_cselect_b64 s[68:69], -1, 0
	s_and_b64 s[66:67], s[66:67], s[68:69]
	s_and_b64 s[68:69], s[66:67], exec
	s_cselect_b32 s68, 0x16c00, 0
	s_or_b32 s90, s88, 15
	s_mov_b32 s69, s72
	s_cmp_ge_i32 s90, s1
	v_lshl_add_u64 v[94:95], v[102:103], 0, s[68:69]
	s_cselect_b64 s[68:69], -1, 0
	s_cmp_lt_i32 s90, s0
	s_cselect_b64 s[70:71], -1, 0
	s_and_b64 s[70:71], s[68:69], s[70:71]
	s_and_b64 s[68:69], s[70:71], exec
	s_cselect_b32 s68, 0x18600, 0
	s_add_i32 s7, s88, 16
	s_mov_b32 s69, s72
	s_cmp_ge_i32 s7, s1
	v_lshl_add_u64 v[96:97], v[102:103], 0, s[68:69]
	s_cselect_b64 s[68:69], -1, 0
	s_cmp_lt_i32 s7, s0
	s_cselect_b64 s[0:1], -1, 0
	s_and_b64 s[68:69], s[68:69], s[0:1]
	s_and_b64 s[0:1], s[68:69], exec
	global_load_ushort v79, v[2:3], off
	global_load_ushort v104, v[4:5], off
	global_load_ushort v105, v[102:103], off
	global_load_ushort v106, v[6:7], off
	global_load_ushort v107, v[8:9], off
	global_load_ushort v108, v[10:11], off
	global_load_ushort v109, v[12:13], off
	s_cselect_b32 s0, 0x1a000, 0
	s_mov_b32 s1, s72
	global_load_ushort v118, v[14:15], off
	global_load_ushort v119, v[16:17], off
	global_load_ushort v120, v[80:81], off
	global_load_ushort v121, v[82:83], off
	global_load_ushort v122, v[84:85], off
	global_load_ushort v123, v[86:87], off
	global_load_ushort v124, v[88:89], off
	global_load_ushort v125, v[90:91], off
	global_load_ushort v126, v[92:93], off
	global_load_ushort v127, v[94:95], off
	global_load_ushort v128, v[96:97], off
	v_lshl_add_u64 v[98:99], v[102:103], 0, s[0:1]
	global_store_dword v[100:101], v34, off offset:3584
	global_load_ushort v129, v[98:99], off
	global_load_dword v117, v[52:53], off
	global_load_dword v116, v[50:51], off
	global_load_dword v133, v[54:55], off
	global_load_dword v134, v[56:57], off
	global_load_dword v136, v[58:59], off
	global_load_ushort v132, v[102:103], off offset:1024
	s_lshl_b64 s[0:1], s[88:89], 11
	s_ashr_i32 s11, s10, 31
	s_ashr_i32 s15, s14, 31
	s_ashr_i32 s7, s6, 31
	s_ashr_i32 s9, s8, 31
	s_ashr_i32 s35, s34, 31
	s_ashr_i32 s37, s36, 31
	s_ashr_i32 s29, s28, 31
	s_ashr_i32 s31, s30, 31
	s_ashr_i32 s25, s24, 31
	s_ashr_i32 s27, s26, 31
	s_ashr_i32 s19, s18, 31
	s_ashr_i32 s23, s22, 31
	s_ashr_i32 s93, s92, 31
	s_ashr_i32 s95, s94, 31
	s_ashr_i32 s91, s90, 31
	s_mov_b32 s97, 0xbfb8aa3b
	s_waitcnt vmcnt(25)
	v_lshlrev_b32_e32 v34, 16, v79
	v_cndmask_b32_e32 v79, 0, v34, vcc
	s_waitcnt vmcnt(24)
	v_lshlrev_b32_e32 v34, 16, v104
	v_cndmask_b32_e64 v115, 0, v34, s[2:3]
	s_waitcnt vmcnt(23)
	v_lshlrev_b32_e32 v34, 16, v105
	v_cndmask_b32_e64 v114, 0, v34, s[4:5]
	s_waitcnt vmcnt(22)
	v_lshlrev_b32_e32 v34, 16, v106
	v_cndmask_b32_e64 v113, 0, v34, s[40:41]
	s_waitcnt vmcnt(21)
	v_lshlrev_b32_e32 v34, 16, v107
	s_waitcnt vmcnt(5)
	v_mul_f32_e32 v101, v117, v115
	s_waitcnt vmcnt(4)
	v_fmac_f32_e32 v101, v116, v79
	v_cndmask_b32_e64 v112, 0, v34, s[42:43]
	v_lshlrev_b32_e32 v34, 16, v108
	s_waitcnt vmcnt(3)
	v_fmac_f32_e32 v101, v133, v114
	v_cndmask_b32_e64 v111, 0, v34, s[44:45]
	v_lshlrev_b32_e32 v34, 16, v109
	s_waitcnt vmcnt(2)
	v_fmac_f32_e32 v101, v134, v113
	v_cndmask_b32_e64 v110, 0, v34, s[46:47]
	v_lshlrev_b32_e32 v34, 16, v118
	s_waitcnt vmcnt(1)
	v_add_f32_e32 v118, v136, v101
	v_mul_f32_e32 v101, 0xbfb8aa3b, v118
	v_cndmask_b32_e64 v109, 0, v34, s[48:49]
	v_lshlrev_b32_e32 v34, 16, v119
	v_exp_f32_e32 v119, v101
	v_cndmask_b32_e64 v108, 0, v34, s[50:51]
	v_lshlrev_b32_e32 v34, 16, v120
	v_mul_f32_e32 v120, v117, v114
	v_fmac_f32_e32 v120, v116, v115
	v_fmac_f32_e32 v120, v133, v113
	v_add_f32_e32 v119, 1.0, v119
	v_fmac_f32_e32 v120, v134, v112
	v_rcp_f32_e32 v119, v119
	v_add_f32_e32 v115, v136, v120
	v_mul_f32_e32 v120, 0xbfb8aa3b, v115
	v_exp_f32_e32 v120, v120
	v_lshlrev_b32_e32 v100, 16, v129
	v_mul_f32_e32 v118, v118, v119
	v_cndmask_b32_e64 v145, 0, v100, s[68:69]
	v_lshl_add_u64 v[100:101], v[60:61], 0, s[0:1]
	v_cvt_pk_bf16_f32 v118, v118, s0
	v_cndmask_b32_e64 v107, 0, v34, s[52:53]
	v_lshlrev_b32_e32 v34, 16, v121
	global_store_short v[100:101], v118, off
	v_add_f32_e32 v118, 1.0, v120
	v_cndmask_b32_e64 v105, 0, v34, s[54:55]
	v_lshlrev_b32_e32 v34, 16, v122
	v_rcp_f32_e32 v118, v118
	v_cndmask_b32_e64 v104, 0, v34, s[56:57]
	v_lshlrev_b32_e32 v34, 16, v123
	v_cndmask_b32_e64 v103, 0, v34, s[58:59]
	v_lshlrev_b32_e32 v34, 16, v124
	v_cndmask_b32_e64 v102, 0, v34, s[60:61]
	v_lshlrev_b32_e32 v34, 16, v125
	v_cndmask_b32_e64 v106, 0, v34, s[62:63]
	v_lshlrev_b32_e32 v34, 16, v126
	s_lshl_b64 s[0:1], s[10:11], 11
	v_mul_f32_e32 v115, v115, v118
	v_cndmask_b32_e64 v138, 0, v34, s[64:65]
	v_lshlrev_b32_e32 v34, 16, v127
	v_lshl_add_u64 v[126:127], v[60:61], 0, s[0:1]
	v_cvt_pk_bf16_f32 v115, v115, s0
	global_store_short v[126:127], v115, off
	v_mul_f32_e32 v115, v117, v113
	v_fmac_f32_e32 v115, v116, v114
	v_fmac_f32_e32 v115, v133, v112
	v_fmac_f32_e32 v115, v134, v111
	v_add_f32_e32 v114, v136, v115
	v_mul_f32_e32 v115, 0xbfb8aa3b, v114
	v_exp_f32_e32 v115, v115
	v_mul_f32_e32 v118, v117, v112
	v_fmac_f32_e32 v118, v116, v113
	v_fmac_f32_e32 v118, v133, v111
	v_add_f32_e32 v115, 1.0, v115
	v_fmac_f32_e32 v118, v134, v110
	v_rcp_f32_e32 v115, v115
	v_add_f32_e32 v113, v136, v118
	v_mul_f32_e32 v118, 0xbfb8aa3b, v113
	v_exp_f32_e32 v118, v118
	s_lshl_b64 s[0:1], s[14:15], 11
	v_mul_f32_e32 v114, v114, v115
	v_lshl_add_u64 v[130:131], v[60:61], 0, s[0:1]
	v_cvt_pk_bf16_f32 v114, v114, s0
	global_store_short v[130:131], v114, off
	v_add_f32_e32 v114, 1.0, v118
	v_rcp_f32_e32 v114, v114
	s_lshl_b64 s[0:1], s[6:7], 11
	v_lshl_add_u64 v[122:123], v[60:61], 0, s[0:1]
	v_cndmask_b32_e64 v140, 0, v34, s[66:67]
	v_mul_f32_e32 v113, v113, v114
	v_cvt_pk_bf16_f32 v113, v113, s0
	global_store_short v[122:123], v113, off
	v_mul_f32_e32 v113, v117, v111
	v_fmac_f32_e32 v113, v116, v112
	v_fmac_f32_e32 v113, v133, v110
	v_fmac_f32_e32 v113, v134, v109
	v_add_f32_e32 v112, v136, v113
	v_mul_f32_e32 v113, 0xbfb8aa3b, v112
	v_exp_f32_e32 v113, v113
	v_mul_f32_e32 v114, v117, v110
	v_fmac_f32_e32 v114, v116, v111
	v_fmac_f32_e32 v114, v133, v109
	v_add_f32_e32 v113, 1.0, v113
	v_fmac_f32_e32 v114, v134, v108
	v_rcp_f32_e32 v113, v113
	v_add_f32_e32 v111, v136, v114
	v_mul_f32_e32 v114, 0xbfb8aa3b, v111
	v_exp_f32_e32 v114, v114
	s_lshl_b64 s[0:1], s[8:9], 11
	v_mul_f32_e32 v112, v112, v113
	v_lshlrev_b32_e32 v34, 16, v128
	v_lshl_add_u64 v[128:129], v[60:61], 0, s[0:1]
	v_cvt_pk_bf16_f32 v112, v112, s0
	global_store_short v[128:129], v112, off
	v_add_f32_e32 v112, 1.0, v114
	v_rcp_f32_e32 v112, v112
	s_lshl_b64 s[0:1], s[34:35], 11
	v_lshl_add_u64 v[118:119], v[60:61], 0, s[0:1]
	v_mul_f32_e32 v146, v117, v106
	v_mul_f32_e32 v111, v111, v112
	v_cvt_pk_bf16_f32 v111, v111, s0
	global_store_short v[118:119], v111, off
	v_mul_f32_e32 v111, v117, v109
	v_fmac_f32_e32 v111, v116, v110
	v_fmac_f32_e32 v111, v133, v108
	v_fmac_f32_e32 v111, v134, v107
	v_add_f32_e32 v110, v136, v111
	v_mul_f32_e32 v111, 0xbfb8aa3b, v110
	v_exp_f32_e32 v111, v111
	v_mul_f32_e32 v112, v117, v108
	v_fmac_f32_e32 v112, v116, v109
	v_fmac_f32_e32 v112, v133, v107
	v_add_f32_e32 v111, 1.0, v111
	v_fmac_f32_e32 v112, v134, v105
	v_rcp_f32_e32 v111, v111
	v_add_f32_e32 v109, v136, v112
	v_mul_f32_e32 v112, 0xbfb8aa3b, v109
	v_exp_f32_e32 v112, v112
	s_lshl_b64 s[0:1], s[36:37], 11
	v_mul_f32_e32 v110, v110, v111
	v_lshl_add_u64 v[124:125], v[60:61], 0, s[0:1]
	v_cvt_pk_bf16_f32 v110, v110, s0
	global_store_short v[124:125], v110, off
	v_add_f32_e32 v110, 1.0, v112
	v_rcp_f32_e32 v110, v110
	s_lshl_b64 s[0:1], s[28:29], 11
	v_lshl_add_u64 v[112:113], v[60:61], 0, s[0:1]
	v_fmac_f32_e32 v146, v116, v102
	v_mul_f32_e32 v109, v109, v110
	v_cvt_pk_bf16_f32 v109, v109, s0
	global_store_short v[112:113], v109, off
	v_mul_f32_e32 v109, v117, v107
	v_fmac_f32_e32 v109, v116, v108
	v_fmac_f32_e32 v109, v133, v105
	v_fmac_f32_e32 v109, v134, v104
	v_add_f32_e32 v108, v136, v109
	v_mul_f32_e32 v109, 0xbfb8aa3b, v108
	v_exp_f32_e32 v109, v109
	v_mul_f32_e32 v110, v117, v105
	v_fmac_f32_e32 v110, v116, v107
	v_fmac_f32_e32 v110, v133, v104
	v_add_f32_e32 v109, 1.0, v109
	v_fmac_f32_e32 v110, v134, v103
	v_rcp_f32_e32 v109, v109
	v_add_f32_e32 v107, v136, v110
	v_mul_f32_e32 v110, 0xbfb8aa3b, v107
	v_exp_f32_e32 v110, v110
	s_lshl_b64 s[0:1], s[30:31], 11
	v_mul_f32_e32 v108, v108, v109
	v_lshl_add_u64 v[120:121], v[60:61], 0, s[0:1]
	v_cvt_pk_bf16_f32 v108, v108, s0
	global_store_short v[120:121], v108, off
	v_add_f32_e32 v108, 1.0, v110
	v_rcp_f32_e32 v110, v108
	s_lshl_b64 s[0:1], s[24:25], 11
	v_lshl_add_u64 v[108:109], v[60:61], 0, s[0:1]
	v_fmac_f32_e32 v146, v133, v138
	v_mul_f32_e32 v107, v107, v110
	v_cvt_pk_bf16_f32 v107, v107, s0
	global_store_short v[108:109], v107, off
	v_mul_f32_e32 v107, v117, v104
	v_fmac_f32_e32 v107, v116, v105
	v_fmac_f32_e32 v107, v133, v103
	v_fmac_f32_e32 v107, v134, v102
	v_add_f32_e32 v105, v136, v107
	v_mul_f32_e32 v110, v117, v103
	v_mul_f32_e32 v107, 0xbfb8aa3b, v105
	v_fmac_f32_e32 v110, v116, v104
	v_exp_f32_e32 v107, v107
	v_fmac_f32_e32 v110, v133, v102
	v_fmac_f32_e32 v110, v134, v106
	v_add_f32_e32 v110, v136, v110
	v_mul_f32_e32 v104, 0xbfb8aa3b, v110
	v_add_f32_e32 v107, 1.0, v107
	v_exp_f32_e32 v104, v104
	v_rcp_f32_e32 v107, v107
	s_lshl_b64 s[0:1], s[26:27], 11
	v_lshl_add_u64 v[114:115], v[60:61], 0, s[0:1]
	v_add_f32_e32 v104, 1.0, v104
	v_mul_f32_e32 v105, v105, v107
	v_rcp_f32_e32 v107, v104
	v_cvt_pk_bf16_f32 v105, v105, s0
	s_lshl_b64 s[0:1], s[18:19], 11
	global_store_short v[114:115], v105, off
	v_mul_f32_e32 v107, v110, v107
	v_lshl_add_u64 v[104:105], v[60:61], 0, s[0:1]
	v_cvt_pk_bf16_f32 v107, v107, s0
	global_store_short v[104:105], v107, off
	v_mul_f32_e32 v107, v117, v102
	v_fmac_f32_e32 v107, v116, v103
	v_fmac_f32_e32 v107, v133, v106
	v_fmac_f32_e32 v107, v134, v138
	v_add_f32_e32 v103, v136, v107
	v_mul_f32_e32 v107, 0xbfb8aa3b, v103
	v_exp_f32_e32 v107, v107
	v_fmac_f32_e32 v146, v134, v140
	v_add_f32_e32 v146, v136, v146
	v_mul_f32_e32 v102, 0xbfb8aa3b, v146
	v_add_f32_e32 v107, 1.0, v107
	v_exp_f32_e32 v102, v102
	v_rcp_f32_e32 v107, v107
	s_lshl_b64 s[0:1], s[22:23], 11
	v_lshl_add_u64 v[110:111], v[60:61], 0, s[0:1]
	v_add_f32_e32 v102, 1.0, v102
	v_mul_f32_e32 v103, v103, v107
	v_rcp_f32_e32 v107, v102
	v_cvt_pk_bf16_f32 v103, v103, s0
	s_lshl_b64 s[0:1], s[92:93], 11
	global_store_short v[110:111], v103, off
	v_mul_f32_e32 v107, v146, v107
	v_lshl_add_u64 v[102:103], v[60:61], 0, s[0:1]
	v_cvt_pk_bf16_f32 v107, v107, s0
	global_store_short v[102:103], v107, off
	v_mul_f32_e32 v107, v117, v138
	v_fmac_f32_e32 v107, v116, v106
	v_mul_f32_e32 v117, v117, v140
	v_cndmask_b32_e64 v144, 0, v34, s[70:71]
	v_fmac_f32_e32 v107, v133, v140
	v_fmac_f32_e32 v117, v116, v138
	v_fmac_f32_e32 v107, v134, v144
	v_fmac_f32_e32 v117, v133, v144
	v_add_f32_e32 v146, v136, v107
	v_fmac_f32_e32 v117, v134, v145
	v_mul_f32_e32 v106, 0xbfb8aa3b, v146
	v_add_f32_e32 v133, v136, v117
	v_exp_f32_e32 v147, v106
	v_mul_f32_e32 v116, 0xbfb8aa3b, v133
	v_exp_f32_e32 v116, v116
	s_lshl_b64 s[0:1], s[94:95], 11
	v_add_f32_e32 v147, 1.0, v147
	v_rcp_f32_e32 v147, v147
	v_add_f32_e32 v116, 1.0, v116
	v_rcp_f32_e32 v134, v116
	v_lshl_add_u64 v[106:107], v[60:61], 0, s[0:1]
	v_mul_f32_e32 v117, v146, v147
	v_cvt_pk_bf16_f32 v117, v117, s0
	s_lshl_b64 s[0:1], s[90:91], 11
	v_mul_f32_e32 v133, v133, v134
	global_store_short v[106:107], v117, off
	v_lshl_add_u64 v[116:117], v[60:61], 0, s[0:1]
	v_cvt_pk_bf16_f32 v133, v133, s0
	global_load_dword v34, v[50:51], off offset:2048
	global_load_dword v79, v[58:59], off offset:2048
	s_nop 0
	global_store_short v[116:117], v133, off
	global_load_ushort v2, v[2:3], off offset:1024
	s_nop 0
	global_load_ushort v3, v[4:5], off offset:1024
	s_nop 0
	global_load_ushort v4, v[6:7], off offset:1024
	global_load_ushort v5, v[8:9], off offset:1024
	s_nop 0
	global_load_ushort v6, v[10:11], off offset:1024
	global_load_ushort v7, v[12:13], off offset:1024
	global_load_ushort v8, v[14:15], off offset:1024
	global_load_ushort v9, v[16:17], off offset:1024
	s_nop 0
	global_load_ushort v10, v[80:81], off offset:1024
	global_load_ushort v11, v[82:83], off offset:1024
	global_load_ushort v12, v[84:85], off offset:1024
	global_load_ushort v13, v[86:87], off offset:1024
	global_load_ushort v14, v[88:89], off offset:1024
	global_load_ushort v15, v[90:91], off offset:1024
	global_load_ushort v16, v[92:93], off offset:1024
	global_load_ushort v17, v[94:95], off offset:1024
	global_load_ushort v80, v[96:97], off offset:1024
	global_load_ushort v81, v[98:99], off offset:1024
	global_load_dword v82, v[62:63], off
	global_load_dword v83, v[64:65], off
	global_load_dword v84, v[66:67], off
	s_waitcnt vmcnt(39)
	v_lshlrev_b32_e32 v85, 16, v132
	v_cndmask_b32_e64 v85, 0, v85, s[4:5]
	s_waitcnt vmcnt(20)
	v_lshlrev_b32_e32 v2, 16, v2
	s_waitcnt vmcnt(19)
	v_lshlrev_b32_e32 v3, 16, v3
	v_cndmask_b32_e64 v3, 0, v3, s[2:3]
	v_cndmask_b32_e32 v2, 0, v2, vcc
	s_waitcnt vmcnt(18)
	v_lshlrev_b32_e32 v4, 16, v4
	v_cndmask_b32_e64 v4, 0, v4, s[40:41]
	s_waitcnt vmcnt(17)
	v_lshlrev_b32_e32 v5, 16, v5
	v_cndmask_b32_e64 v5, 0, v5, s[42:43]
	s_waitcnt vmcnt(16)
	v_lshlrev_b32_e32 v6, 16, v6
	v_cndmask_b32_e64 v6, 0, v6, s[44:45]
	s_waitcnt vmcnt(15)
	v_lshlrev_b32_e32 v7, 16, v7
	v_cndmask_b32_e64 v7, 0, v7, s[46:47]
	s_waitcnt vmcnt(14)
	v_lshlrev_b32_e32 v8, 16, v8
	v_cndmask_b32_e64 v8, 0, v8, s[48:49]
	s_waitcnt vmcnt(13)
	v_lshlrev_b32_e32 v9, 16, v9
	v_cndmask_b32_e64 v9, 0, v9, s[50:51]
	s_waitcnt vmcnt(12)
	v_lshlrev_b32_e32 v10, 16, v10
	v_cndmask_b32_e64 v10, 0, v10, s[52:53]
	s_waitcnt vmcnt(2)
	v_mul_f32_e32 v86, v82, v3
	v_fmac_f32_e32 v86, v34, v2
	s_waitcnt vmcnt(1)
	v_fmac_f32_e32 v86, v83, v85
	v_mul_f32_e32 v87, v82, v85
	s_waitcnt vmcnt(0)
	v_fmac_f32_e32 v86, v84, v4
	v_fmac_f32_e32 v87, v34, v3
	v_add_f32_e32 v2, v79, v86
	v_fmac_f32_e32 v87, v83, v4
	v_mul_f32_e32 v86, 0xbfb8aa3b, v2
	v_fmac_f32_e32 v87, v84, v5
	v_exp_f32_e32 v86, v86
	v_add_f32_e32 v3, v79, v87
	v_mul_f32_e32 v87, 0xbfb8aa3b, v3
	v_exp_f32_e32 v87, v87
	v_add_f32_e32 v86, 1.0, v86
	v_rcp_f32_e32 v86, v86
	v_lshlrev_b32_e32 v11, 16, v11
	v_add_f32_e32 v87, 1.0, v87
	v_rcp_f32_e32 v87, v87
	v_mul_f32_e32 v2, v2, v86
	v_cvt_pk_bf16_f32 v2, v2, s0
	global_store_short v[100:101], v2, off offset:1024
	v_mul_f32_e32 v2, v3, v87
	v_mul_f32_e32 v3, v82, v4
	v_fmac_f32_e32 v3, v34, v85
	v_fmac_f32_e32 v3, v83, v5
	v_fmac_f32_e32 v3, v84, v6
	v_add_f32_e32 v3, v79, v3
	v_mul_f32_e32 v85, 0xbfb8aa3b, v3
	v_exp_f32_e32 v85, v85
	v_mul_f32_e32 v86, v82, v5
	v_fmac_f32_e32 v86, v34, v4
	v_fmac_f32_e32 v86, v83, v6
	v_fmac_f32_e32 v86, v84, v7
	v_add_f32_e32 v85, 1.0, v85
	v_add_f32_e32 v4, v79, v86
	v_rcp_f32_e32 v85, v85
	v_mul_f32_e32 v86, 0xbfb8aa3b, v4
	v_exp_f32_e32 v86, v86
	v_cvt_pk_bf16_f32 v2, v2, s0
	v_mul_f32_e32 v3, v3, v85
	v_cvt_pk_bf16_f32 v3, v3, s0
	global_store_short v[126:127], v2, off offset:1024
	v_add_f32_e32 v2, 1.0, v86
	global_store_short v[130:131], v3, off offset:1024
	v_mul_f32_e32 v3, v82, v6
	v_rcp_f32_e32 v2, v2
	v_fmac_f32_e32 v3, v34, v5
	v_fmac_f32_e32 v3, v83, v7
	v_fmac_f32_e32 v3, v84, v8
	v_add_f32_e32 v3, v79, v3
	v_mul_f32_e32 v2, v4, v2
	v_mul_f32_e32 v4, 0xbfb8aa3b, v3
	v_exp_f32_e32 v4, v4
	v_mul_f32_e32 v5, v82, v7
	v_fmac_f32_e32 v5, v34, v6
	v_fmac_f32_e32 v5, v83, v8
	v_add_f32_e32 v4, 1.0, v4
	v_rcp_f32_e32 v4, v4
	v_fmac_f32_e32 v5, v84, v9
	v_add_f32_e32 v5, v79, v5
	v_mul_f32_e32 v6, 0xbfb8aa3b, v5
	v_mul_f32_e32 v3, v3, v4
	v_exp_f32_e32 v6, v6
	v_cvt_pk_bf16_f32 v3, v3, s0
	global_store_short v[128:129], v3, off offset:1024
	v_mul_f32_e32 v3, v82, v8
	v_fmac_f32_e32 v3, v34, v7
	v_cvt_pk_bf16_f32 v2, v2, s0
	v_fmac_f32_e32 v3, v83, v9
	global_store_short v[122:123], v2, off offset:1024
	v_add_f32_e32 v2, 1.0, v6
	v_fmac_f32_e32 v3, v84, v10
	v_rcp_f32_e32 v2, v2
	v_add_f32_e32 v3, v79, v3
	v_mul_f32_e32 v4, 0xbfb8aa3b, v3
	v_exp_f32_e32 v4, v4
	v_mul_f32_e32 v2, v5, v2
	v_mul_f32_e32 v5, v82, v9
	v_fmac_f32_e32 v5, v34, v8
	v_cndmask_b32_e64 v11, 0, v11, s[54:55]
	v_fmac_f32_e32 v5, v83, v10
	v_add_f32_e32 v4, 1.0, v4
	v_fmac_f32_e32 v5, v84, v11
	v_rcp_f32_e32 v4, v4
	v_add_f32_e32 v5, v79, v5
	v_mul_f32_e32 v6, 0xbfb8aa3b, v5
	v_exp_f32_e32 v6, v6
	v_mul_f32_e32 v3, v3, v4
	v_cvt_pk_bf16_f32 v3, v3, s0
	v_cvt_pk_bf16_f32 v2, v2, s0
	global_store_short v[124:125], v3, off offset:1024
	v_mul_f32_e32 v3, v82, v10
	v_lshlrev_b32_e32 v12, 16, v12
	global_store_short v[118:119], v2, off offset:1024
	v_add_f32_e32 v2, 1.0, v6
	v_fmac_f32_e32 v3, v34, v9
	v_cndmask_b32_e64 v12, 0, v12, s[56:57]
	v_rcp_f32_e32 v2, v2
	v_fmac_f32_e32 v3, v83, v11
	v_fmac_f32_e32 v3, v84, v12
	v_add_f32_e32 v3, v79, v3
	v_mul_f32_e32 v4, 0xbfb8aa3b, v3
	v_mul_f32_e32 v2, v5, v2
	v_exp_f32_e32 v4, v4
	v_mul_f32_e32 v5, v82, v11
	v_lshlrev_b32_e32 v13, 16, v13
	v_fmac_f32_e32 v5, v34, v10
	v_cndmask_b32_e64 v13, 0, v13, s[58:59]
	v_fmac_f32_e32 v5, v83, v12
	v_fmac_f32_e32 v5, v84, v13
	v_add_f32_e32 v5, v79, v5
	v_add_f32_e32 v4, 1.0, v4
	v_mul_f32_e32 v6, 0xbfb8aa3b, v5
	v_rcp_f32_e32 v4, v4
	v_exp_f32_e32 v6, v6
	v_cvt_pk_bf16_f32 v2, v2, s0
	global_store_short v[112:113], v2, off offset:1024
	v_mul_f32_e32 v3, v3, v4
	v_add_f32_e32 v2, 1.0, v6
	v_cvt_pk_bf16_f32 v3, v3, s0
	v_rcp_f32_e32 v2, v2
	global_store_short v[120:121], v3, off offset:1024
	v_mul_f32_e32 v3, v82, v12
	v_lshlrev_b32_e32 v14, 16, v14
	v_fmac_f32_e32 v3, v34, v11
	v_cndmask_b32_e64 v14, 0, v14, s[60:61]
	v_fmac_f32_e32 v3, v83, v13
	v_fmac_f32_e32 v3, v84, v14
	v_mul_f32_e32 v2, v5, v2
	v_add_f32_e32 v3, v79, v3
	v_mul_f32_e32 v5, v82, v13
	v_lshlrev_b32_e32 v15, 16, v15
	v_mul_f32_e32 v4, 0xbfb8aa3b, v3
	v_fmac_f32_e32 v5, v34, v12
	v_cndmask_b32_e64 v15, 0, v15, s[62:63]
	v_exp_f32_e32 v4, v4
	v_fmac_f32_e32 v5, v83, v14
	v_fmac_f32_e32 v5, v84, v15
	v_add_f32_e32 v5, v79, v5
	v_mul_f32_e32 v6, 0xbfb8aa3b, v5
	v_exp_f32_e32 v6, v6
	v_add_f32_e32 v4, 1.0, v4
	v_rcp_f32_e32 v4, v4
	v_cvt_pk_bf16_f32 v2, v2, s0
	global_store_short v[108:109], v2, off offset:1024
	v_add_f32_e32 v2, 1.0, v6
	v_rcp_f32_e32 v2, v2
	v_mul_f32_e32 v3, v3, v4
	v_cvt_pk_bf16_f32 v3, v3, s0
	global_store_short v[114:115], v3, off offset:1024
	v_mul_f32_e32 v3, v82, v14
	v_lshlrev_b32_e32 v16, 16, v16
	v_fmac_f32_e32 v3, v34, v13
	v_cndmask_b32_e64 v16, 0, v16, s[64:65]
	v_mul_f32_e32 v2, v5, v2
	v_fmac_f32_e32 v3, v83, v15
	v_mul_f32_e32 v5, v82, v15
	v_lshlrev_b32_e32 v17, 16, v17
	v_fmac_f32_e32 v3, v84, v16
	v_fmac_f32_e32 v5, v34, v14
	v_cndmask_b32_e64 v17, 0, v17, s[66:67]
	v_add_f32_e32 v3, v79, v3
	v_fmac_f32_e32 v5, v83, v16
	v_mul_f32_e32 v4, 0xbfb8aa3b, v3
	v_fmac_f32_e32 v5, v84, v17
	v_exp_f32_e32 v4, v4
	v_add_f32_e32 v5, v79, v5
	v_mul_f32_e32 v6, 0xbfb8aa3b, v5
	v_exp_f32_e32 v6, v6
	v_add_f32_e32 v4, 1.0, v4
	v_cvt_pk_bf16_f32 v2, v2, s0
	v_rcp_f32_e32 v4, v4
	global_store_short v[104:105], v2, off offset:1024
	v_add_f32_e32 v2, 1.0, v6
	v_rcp_f32_e32 v2, v2
	v_mul_f32_e32 v3, v3, v4
	v_cvt_pk_bf16_f32 v3, v3, s0
	v_lshlrev_b32_e32 v80, 16, v80
	global_store_short v[110:111], v3, off offset:1024
	v_mul_f32_e32 v2, v5, v2
	v_mul_f32_e32 v3, v82, v16
	v_mul_f32_e32 v5, v82, v17
	v_cndmask_b32_e64 v80, 0, v80, s[70:71]
	v_lshlrev_b32_e32 v81, 16, v81
	v_fmac_f32_e32 v3, v34, v15
	v_fmac_f32_e32 v5, v34, v16
	v_cndmask_b32_e64 v81, 0, v81, s[68:69]
	v_fmac_f32_e32 v3, v83, v17
	v_fmac_f32_e32 v5, v83, v80
	v_fmac_f32_e32 v3, v84, v80
	v_fmac_f32_e32 v5, v84, v81
	v_add_f32_e32 v3, v79, v3
	v_add_f32_e32 v5, v79, v5
	v_mul_f32_e32 v4, 0xbfb8aa3b, v3
	v_mul_f32_e32 v6, 0xbfb8aa3b, v5
	v_exp_f32_e32 v4, v4
	v_exp_f32_e32 v6, v6
	v_cvt_pk_bf16_f32 v2, v2, s0
	global_store_short v[102:103], v2, off offset:1024
	v_add_f32_e32 v4, 1.0, v4
	v_add_f32_e32 v2, 1.0, v6
	v_rcp_f32_e32 v4, v4
	v_rcp_f32_e32 v2, v2
	v_mul_f32_e32 v3, v3, v4
	v_mul_f32_e32 v2, v5, v2
	v_cvt_pk_bf16_f32 v3, v3, s0
	v_cvt_pk_bf16_f32 v2, v2, s0
	global_store_short v[106:107], v3, off offset:1024
	global_store_short v[116:117], v2, off offset:1024
	s_and_saveexec_b64 s[0:1], s[38:39]
	s_movk_i32 s90, 0x1a00
	s_cbranch_execz .LBB0_247
	v_readlane_b32 s2, v255, 48
	v_readlane_b32 s3, v255, 49
	v_add_u32_e32 v2, s88, v19
	v_mov_b32_e32 v79, v35
	v_mov_b64_e32 v[4:5], s[2:3]
	v_mad_i64_i32 v[4:5], s[2:3], v2, s90, v[4:5]
	v_lshl_add_u64 v[4:5], v[4:5], 0, v[78:79]
	v_add_co_u32_e32 v4, vcc, 0x1000, v4
	s_nop 1
	v_addc_co_u32_e32 v5, vcc, 0, v5, vcc
	global_load_ushort v3, v[4:5], off offset:2432
	s_nop 0
	global_load_dword v4, v[68:69], off
	s_waitcnt vmcnt(1)
	v_lshlrev_b32_e32 v3, 16, v3
	s_waitcnt vmcnt(0)
	v_add_f32_e32 v4, v4, v3
	v_mul_f32_e64 v3, |v4|, s97
	v_exp_f32_e32 v3, v3
	v_max_f32_e32 v4, 0, v4
	v_add_f32_e32 v3, 1.0, v3
	v_log_f32_e32 v5, v3
	v_ashrrev_i32_e32 v3, 31, v2
	v_lshlrev_b64 v[2:3], 6, v[2:3]
	v_lshl_add_u64 v[2:3], v[70:71], 0, v[2:3]
	v_fmac_f32_e32 v4, 0x3f317218, v5
	global_store_dword v[2:3], v4, off
	s_branch .LBB0_247
